# pass C software-pipelined two tokens deep; unnormalised rows written in place in the output buffer (no scratch copy)
# baseline (speedup 1.0000x reference)
.Lgbb_1444:
	s_or_b64 exec, exec, s[2:3]
	s_waitcnt lgkmcnt(0)
	s_barrier
	s_mov_b64 exec, -1
	v_and_b32_e32 v1, 63, v0
	v_readfirstlane_b32 s16, v0
	s_load_dwordx2 s[12:13], s[0:1], 0xc0
	s_lshr_b32 s16, s16, 6
	s_and_b32 s18, s33, 7
	s_lshr_b32 s19, s33, 3
	s_lshl_b32 s19, s19, 8
	s_lshl_b32 s16, s16, 5
	s_add_i32 s16, s16, s19
	s_add_i32 s17, s16, 32
	s_add_i32 s24, s17, -1
	s_lshl_b32 s19, s18, 9
	v_lshl_add_u32 v162, v1, 3, s19
	v_mov_b32_e32 v163, 0
	s_mov_b32 s31, 0
	v_mov_b32_e32 v4, v1
	v_mov_b32_e32 v5, 0
	s_mov_b32 s69, 0
	s_mov_b32 s68, 0x400000
	s_mov_b32 s41, 0x378e98ab
	s_mov_b32 s42, 0x3b7cd369
	s_mov_b32 s43, 0xbcc618b2
	s_mov_b32 s44, 0x3dda74e4
	s_mov_b32 s45, 0x3f228afd
	s_mov_b32 s46, 0x3e03c728
	s_mov_b32 s47, 0xbfb8aa3b
	s_mov_b32 s48, 0x42ce8ed0
	s_mov_b32 s49, 0xc2b17218
	s_mov_b32 s50, 0x7fffffff
	v_mov_b32_e32 v97, 0x43000000
	v_mov_b32_e32 v250, 0x3ba10414
	v_mov_b32_e32 v251, 0xb9c68948
	v_mov_b32_e32 v252, 0x7f800000
	s_load_dwordx2 s[4:5], s[0:1], 0xb8
	s_waitcnt lgkmcnt(0)
	s_add_u32 s26, s12, 0x17c00000
	s_addc_u32 s27, s13, 0
	s_add_u32 s20, s12, 0x100000
	s_addc_u32 s21, s13, 0
	v_lshl_add_u64 v[172:173], v[162:163], 1, s[20:21]
	s_add_u32 s20, s12, 0x4da00000
	s_addc_u32 s21, s13, 0
	v_lshl_add_u64 v[174:175], v[4:5], 2, s[20:21]
	s_add_u32 s20, s12, 0x4de00000
	s_addc_u32 s21, s13, 0
	v_lshl_add_u64 v[176:177], v[4:5], 2, s[20:21]
	s_add_u32 s20, s12, 0x23c00000
	s_addc_u32 s21, s13, 0
	v_lshl_add_u64 v[210:211], v[4:5], 2, s[20:21]
	s_add_u32 s20, s12, 0x25c00000
	s_addc_u32 s21, s13, 0
	v_and_b32_e32 v6, 7, v1
	v_mov_b32_e32 v7, 0
	v_lshlrev_b32_e32 v6, 20, v6
	v_lshl_add_u64 v[212:213], v[6:7], 0, s[20:21]
	v_lshl_add_u64 v[214:215], v[162:163], 2, s[4:5]
	s_add_u32 s66, s12, 0x1fe00000
	s_addc_u32 s67, s13, 0
	s_add_u32 s64, s12, 0x38d80000
	s_addc_u32 s65, s13, 0
	s_add_u32 s60, s12, 0x38d90000
	s_addc_u32 s61, s13, 0
	s_lshl_b32 s19, s18, 20
	s_add_u32 s62, s12, 0x26c00000
	s_addc_u32 s63, s13, 0
	s_add_u32 s62, s62, s19
	s_addc_u32 s63, s63, 0
	v_mov_b32_e32 v19, 0
	s_mov_b32 s2, 0x55555555
	s_mov_b32 s3, 0x55555555
	s_lshl_b32 s30, s16, 13
	v_lshl_add_u64 v[160:161], v[172:173], 0, s[30:31]
	global_load_dwordx4 v[116:119], v[160:161], off
	s_lshl_b32 s30, s16, 9
	v_lshl_add_u64 v[160:161], v[174:175], 0, s[30:31]
	global_load_dword v122, v[160:161], off
	global_load_dword v123, v[160:161], off offset:256
	v_lshl_add_u64 v[160:161], v[176:177], 0, s[30:31]
	global_load_dword v216, v[160:161], off
	global_load_dword v217, v[160:161], off offset:256
	v_lshl_add_u64 v[160:161], v[210:211], 0, s[30:31]
	global_load_dword v218, v[160:161], off
	global_load_dword v226, v[160:161], off offset:256
	v_lshl_add_u64 v[160:161], v[160:161], 0, s[68:69]
	global_load_dword v219, v[160:161], off
	global_load_dword v227, v[160:161], off offset:256
	v_lshl_add_u64 v[160:161], v[160:161], 0, s[68:69]
	global_load_dword v220, v[160:161], off
	global_load_dword v228, v[160:161], off offset:256
	v_lshl_add_u64 v[160:161], v[160:161], 0, s[68:69]
	global_load_dword v221, v[160:161], off
	global_load_dword v229, v[160:161], off offset:256
	v_lshl_add_u64 v[160:161], v[160:161], 0, s[68:69]
	global_load_dword v222, v[160:161], off
	global_load_dword v230, v[160:161], off offset:256
	v_lshl_add_u64 v[160:161], v[160:161], 0, s[68:69]
	global_load_dword v223, v[160:161], off
	global_load_dword v231, v[160:161], off offset:256
	v_lshl_add_u64 v[160:161], v[160:161], 0, s[68:69]
	global_load_dword v224, v[160:161], off
	global_load_dword v232, v[160:161], off offset:256
	v_lshl_add_u64 v[160:161], v[160:161], 0, s[68:69]
	global_load_dword v225, v[160:161], off
	global_load_dword v233, v[160:161], off offset:256
	s_lshl_b32 s30, s16, 7
	v_lshl_add_u64 v[160:161], v[212:213], 0, s[30:31]
	global_load_dword v234, v[160:161], off
	s_lshl_b32 s30, s16, 2
	s_add_u32 s28, s66, s30
	s_addc_u32 s29, s67, 0
	global_load_dword v235, v19, s[28:29]
	s_waitcnt vmcnt(0)
	v_lshlrev_b32_e32 v16, 2, v122
	v_lshlrev_b32_e32 v17, 2, v123
	global_load_dword v238, v16, s[64:65]
	global_load_dword v240, v16, s[60:61]
	global_load_dword v239, v17, s[64:65]
	global_load_dword v241, v17, s[60:61]
	s_waitcnt vmcnt(0)
	v_readlane_b32 s30, v122, 0
	s_lshl_b32 s30, s30, 12
	s_add_u32 s28, s26, s30
	s_addc_u32 s29, s27, 0
	global_load_dwordx2 v[24:25], v162, s[28:29]
	v_readlane_b32 s30, v122, 1
	s_lshl_b32 s30, s30, 12
	s_add_u32 s28, s26, s30
	s_addc_u32 s29, s27, 0
	global_load_dwordx2 v[26:27], v162, s[28:29]
	v_readlane_b32 s30, v122, 2
	s_lshl_b32 s30, s30, 12
	s_add_u32 s28, s26, s30
	s_addc_u32 s29, s27, 0
	global_load_dwordx2 v[28:29], v162, s[28:29]
	v_readlane_b32 s30, v122, 3
	s_lshl_b32 s30, s30, 12
	s_add_u32 s28, s26, s30
	s_addc_u32 s29, s27, 0
	global_load_dwordx2 v[30:31], v162, s[28:29]
	v_readlane_b32 s30, v122, 4
	s_lshl_b32 s30, s30, 12
	s_add_u32 s28, s26, s30
	s_addc_u32 s29, s27, 0
	global_load_dwordx2 v[32:33], v162, s[28:29]
	v_readlane_b32 s30, v122, 5
	s_lshl_b32 s30, s30, 12
	s_add_u32 s28, s26, s30
	s_addc_u32 s29, s27, 0
	global_load_dwordx2 v[34:35], v162, s[28:29]
	v_readlane_b32 s30, v122, 6
	s_lshl_b32 s30, s30, 12
	s_add_u32 s28, s26, s30
	s_addc_u32 s29, s27, 0
	global_load_dwordx2 v[36:37], v162, s[28:29]
	v_readlane_b32 s30, v122, 7
	s_lshl_b32 s30, s30, 12
	s_add_u32 s28, s26, s30
	s_addc_u32 s29, s27, 0
	global_load_dwordx2 v[38:39], v162, s[28:29]
	v_readlane_b32 s30, v122, 8
	s_lshl_b32 s30, s30, 12
	s_add_u32 s28, s26, s30
	s_addc_u32 s29, s27, 0
	global_load_dwordx2 v[40:41], v162, s[28:29]
	v_readlane_b32 s30, v122, 9
	s_lshl_b32 s30, s30, 12
	s_add_u32 s28, s26, s30
	s_addc_u32 s29, s27, 0
	global_load_dwordx2 v[42:43], v162, s[28:29]
	v_readlane_b32 s30, v122, 10
	s_lshl_b32 s30, s30, 12
	s_add_u32 s28, s26, s30
	s_addc_u32 s29, s27, 0
	global_load_dwordx2 v[44:45], v162, s[28:29]
	v_readlane_b32 s30, v122, 11
	s_lshl_b32 s30, s30, 12
	s_add_u32 s28, s26, s30
	s_addc_u32 s29, s27, 0
	global_load_dwordx2 v[46:47], v162, s[28:29]
	v_readlane_b32 s30, v122, 12
	s_lshl_b32 s30, s30, 12
	s_add_u32 s28, s26, s30
	s_addc_u32 s29, s27, 0
	global_load_dwordx2 v[48:49], v162, s[28:29]
	v_readlane_b32 s30, v122, 13
	s_lshl_b32 s30, s30, 12
	s_add_u32 s28, s26, s30
	s_addc_u32 s29, s27, 0
	global_load_dwordx2 v[50:51], v162, s[28:29]
	v_readlane_b32 s30, v122, 14
	s_lshl_b32 s30, s30, 12
	s_add_u32 s28, s26, s30
	s_addc_u32 s29, s27, 0
	global_load_dwordx2 v[52:53], v162, s[28:29]
	v_readlane_b32 s30, v122, 15
	s_lshl_b32 s30, s30, 12
	s_add_u32 s28, s26, s30
	s_addc_u32 s29, s27, 0
	global_load_dwordx2 v[54:55], v162, s[28:29]
	v_readlane_b32 s30, v122, 16
	s_lshl_b32 s30, s30, 12
	s_add_u32 s28, s26, s30
	s_addc_u32 s29, s27, 0
	global_load_dwordx2 v[56:57], v162, s[28:29]
	v_readlane_b32 s30, v122, 17
	s_lshl_b32 s30, s30, 12
	s_add_u32 s28, s26, s30
	s_addc_u32 s29, s27, 0
	global_load_dwordx2 v[58:59], v162, s[28:29]
	v_readlane_b32 s30, v122, 18
	s_lshl_b32 s30, s30, 12
	s_add_u32 s28, s26, s30
	s_addc_u32 s29, s27, 0
	global_load_dwordx2 v[60:61], v162, s[28:29]
	v_readlane_b32 s30, v122, 19
	s_lshl_b32 s30, s30, 12
	s_add_u32 s28, s26, s30
	s_addc_u32 s29, s27, 0
	global_load_dwordx2 v[62:63], v162, s[28:29]
	v_readlane_b32 s30, v122, 20
	s_lshl_b32 s30, s30, 12
	s_add_u32 s28, s26, s30
	s_addc_u32 s29, s27, 0
	global_load_dwordx2 v[64:65], v162, s[28:29]
	v_readlane_b32 s30, v122, 21
	s_lshl_b32 s30, s30, 12
	s_add_u32 s28, s26, s30
	s_addc_u32 s29, s27, 0
	global_load_dwordx2 v[66:67], v162, s[28:29]
	v_readlane_b32 s30, v122, 22
	s_lshl_b32 s30, s30, 12
	s_add_u32 s28, s26, s30
	s_addc_u32 s29, s27, 0
	global_load_dwordx2 v[68:69], v162, s[28:29]
	v_readlane_b32 s30, v122, 23
	s_lshl_b32 s30, s30, 12
	s_add_u32 s28, s26, s30
	s_addc_u32 s29, s27, 0
	global_load_dwordx2 v[70:71], v162, s[28:29]
	v_readlane_b32 s30, v122, 24
	s_lshl_b32 s30, s30, 12
	s_add_u32 s28, s26, s30
	s_addc_u32 s29, s27, 0
	global_load_dwordx2 v[72:73], v162, s[28:29]
	v_readlane_b32 s30, v122, 25
	s_lshl_b32 s30, s30, 12
	s_add_u32 s28, s26, s30
	s_addc_u32 s29, s27, 0
	global_load_dwordx2 v[74:75], v162, s[28:29]
	v_readlane_b32 s30, v122, 26
	s_lshl_b32 s30, s30, 12
	s_add_u32 s28, s26, s30
	s_addc_u32 s29, s27, 0
	global_load_dwordx2 v[76:77], v162, s[28:29]
	v_readlane_b32 s30, v122, 27
	s_lshl_b32 s30, s30, 12
	s_add_u32 s28, s26, s30
	s_addc_u32 s29, s27, 0
	global_load_dwordx2 v[78:79], v162, s[28:29]
	v_readlane_b32 s30, v122, 28
	s_lshl_b32 s30, s30, 12
	s_add_u32 s28, s26, s30
	s_addc_u32 s29, s27, 0
	global_load_dwordx2 v[80:81], v162, s[28:29]
	v_readlane_b32 s30, v122, 29
	s_lshl_b32 s30, s30, 12
	s_add_u32 s28, s26, s30
	s_addc_u32 s29, s27, 0
	global_load_dwordx2 v[82:83], v162, s[28:29]
	v_readlane_b32 s30, v122, 30
	s_lshl_b32 s30, s30, 12
	s_add_u32 s28, s26, s30
	s_addc_u32 s29, s27, 0
	global_load_dwordx2 v[84:85], v162, s[28:29]
	v_readlane_b32 s30, v122, 31
	s_lshl_b32 s30, s30, 12
	s_add_u32 s28, s26, s30
	s_addc_u32 s29, s27, 0
	global_load_dwordx2 v[86:87], v162, s[28:29]

.Lgbc_1444:
	s_or_b64 exec, exec, s[2:3]
	s_waitcnt lgkmcnt(0)
	s_barrier
	s_mov_b64 exec, -1
	s_load_dwordx2 s[12:13], s[0:1], 0xc0
	s_load_dwordx2 s[4:5], s[0:1], 0xb8
	s_load_dwordx2 s[6:7], s[0:1], 0xb0
	v_lshlrev_b32_e32 v2, 5, v0
	v_mov_b32_e32 v3, 0
	v_mov_b32_e32 v173, 0x358637bd
	v_mov_b32_e32 v174, 0x260
	s_mov_b32 s51, 0xf800000
	s_mov_b32 s31, 0
	s_lshl_b32 s16, s33, 5
	s_waitcnt lgkmcnt(0)
	v_lshl_add_u64 v[4:5], v[2:3], 0, s[6:7]
	global_load_dwordx4 v[100:103], v[4:5], off
	global_load_dwordx4 v[104:107], v[4:5], off offset:16
	s_lshl_b32 s30, s16, 14
	v_lshl_add_u64 v[6:7], v[2:3], 0, s[4:5]
	v_lshl_add_u64 v[6:7], v[6:7], 0, s[30:31]
	v_mov_b32_e32 v32, v6
	v_mov_b32_e32 v33, v7
	s_add_u32 s62, s12, 0x26c00000
	s_addc_u32 s63, s13, 0
	v_and_b32_e32 v8, 7, v0
	v_mov_b32_e32 v9, 0
	v_lshlrev_b32_e32 v8, 20, v8
	v_lshl_add_u64 v[26:27], v[8:9], 0, s[62:63]
	s_lshl_b32 s30, s16, 7
	v_lshl_add_u64 v[26:27], v[26:27], 0, s[30:31]
	s_mov_b32 s30, 0x4000
	s_mov_b32 s28, 0x80
	s_mov_b32 s29, 0
	global_load_dwordx4 v[10:13], v[32:33], off
	global_load_dwordx4 v[14:17], v[32:33], off offset:16
	global_load_dword v45, v[26:27], off
	v_lshl_add_u64 v[32:33], v[32:33], 0, s[30:31]
	v_lshl_add_u64 v[26:27], v[26:27], 0, s[28:29]
	global_load_dwordx4 v[36:39], v[32:33], off
	global_load_dwordx4 v[40:43], v[32:33], off offset:16
	global_load_dword v44, v[26:27], off
	v_lshl_add_u64 v[32:33], v[32:33], 0, s[30:31]
	v_lshl_add_u64 v[26:27], v[26:27], 0, s[28:29]
	s_waitcnt vmcnt(3)
	s_nop 1
	v_add_f32_dpp v19, v45, v45 quad_perm:[1,0,3,2] row_mask:0xf bank_mask:0xf
	s_nop 1
	v_add_f32_dpp v18, v19, v19 quad_perm:[2,3,0,1] row_mask:0xf bank_mask:0xf
	s_nop 1
	v_add_f32_dpp v18, v18, v18 row_half_mirror row_mask:0xf bank_mask:0xf
	v_fmamk_f32 v18, v18, 0x39800000, v173
	v_mul_f32_e32 v19, 0x4f800000, v18
	v_cmp_gt_f32_e32 vcc, s51, v18
	s_nop 1
	v_cndmask_b32_e32 v18, v18, v19, vcc
	v_sqrt_f32_e32 v19, v18
	s_nop 0
	v_add_u32_e32 v20, -1, v19
	v_fma_f32 v22, -v20, v19, v18
	v_add_u32_e32 v21, 1, v19
	v_cmp_ge_f32_e64 s[14:15], 0, v22
	s_nop 1
	v_cndmask_b32_e64 v20, v19, v20, s[14:15]
	v_fma_f32 v19, -v21, v19, v18
	v_cmp_lt_f32_e64 s[14:15], 0, v19
	s_nop 1
	v_cndmask_b32_e64 v19, v20, v21, s[14:15]
	v_mul_f32_e32 v20, 0x37800000, v19
	v_cndmask_b32_e32 v19, v19, v20, vcc
	v_cmp_class_f32_e32 vcc, v18, v174
	s_nop 1
	v_cndmask_b32_e32 v18, v19, v18, vcc
	v_div_scale_f32 v19, s[14:15], v18, v18, 1.0
	v_rcp_f32_e32 v20, v19
	s_nop 0
	v_fma_f32 v21, -v19, v20, 1.0
	v_fmac_f32_e32 v20, v21, v20
	v_div_scale_f32 v21, vcc, 1.0, v18, 1.0
	v_mul_f32_e32 v22, v21, v20
	v_fma_f32 v23, -v19, v22, v21
	v_fmac_f32_e32 v22, v23, v20
	v_fma_f32 v19, -v19, v22, v21
	v_div_fmas_f32 v19, v19, v20, v22
	v_div_fixup_f32 v18, v19, v18, 1.0
	v_pk_mul_f32 v[10:11], v[10:11], v[18:19] op_sel_hi:[1,0]
	v_pk_mul_f32 v[12:13], v[12:13], v[18:19] op_sel_hi:[1,0]
	v_pk_mul_f32 v[14:15], v[14:15], v[18:19] op_sel_hi:[1,0]
	v_pk_mul_f32 v[16:17], v[16:17], v[18:19] op_sel_hi:[1,0]
	v_pk_mul_f32 v[10:11], v[10:11], v[100:101]
	v_pk_mul_f32 v[12:13], v[12:13], v[102:103]
	v_pk_mul_f32 v[14:15], v[14:15], v[104:105]
	v_pk_mul_f32 v[16:17], v[16:17], v[106:107]
	global_store_dwordx4 v[6:7], v[10:13], off
	global_store_dwordx4 v[6:7], v[14:17], off offset:16
	v_lshl_add_u64 v[6:7], v[6:7], 0, s[30:31]
	global_load_dwordx4 v[10:13], v[32:33], off
	global_load_dwordx4 v[14:17], v[32:33], off offset:16
	global_load_dword v45, v[26:27], off
	v_lshl_add_u64 v[32:33], v[32:33], 0, s[30:31]
	v_lshl_add_u64 v[26:27], v[26:27], 0, s[28:29]
	s_waitcnt vmcnt(3)
	s_nop 1
	v_add_f32_dpp v19, v44, v44 quad_perm:[1,0,3,2] row_mask:0xf bank_mask:0xf
	s_nop 1
	v_add_f32_dpp v18, v19, v19 quad_perm:[2,3,0,1] row_mask:0xf bank_mask:0xf
	s_nop 1
	v_add_f32_dpp v18, v18, v18 row_half_mirror row_mask:0xf bank_mask:0xf
	v_fmamk_f32 v18, v18, 0x39800000, v173
	v_mul_f32_e32 v19, 0x4f800000, v18
	v_cmp_gt_f32_e32 vcc, s51, v18
	s_nop 1
	v_cndmask_b32_e32 v18, v18, v19, vcc
	v_sqrt_f32_e32 v19, v18
	s_nop 0
	v_add_u32_e32 v20, -1, v19
	v_fma_f32 v22, -v20, v19, v18
	v_add_u32_e32 v21, 1, v19
	v_cmp_ge_f32_e64 s[14:15], 0, v22
	s_nop 1
	v_cndmask_b32_e64 v20, v19, v20, s[14:15]
	v_fma_f32 v19, -v21, v19, v18
	v_cmp_lt_f32_e64 s[14:15], 0, v19
	s_nop 1
	v_cndmask_b32_e64 v19, v20, v21, s[14:15]
	v_mul_f32_e32 v20, 0x37800000, v19
	v_cndmask_b32_e32 v19, v19, v20, vcc
	v_cmp_class_f32_e32 vcc, v18, v174
	s_nop 1
	v_cndmask_b32_e32 v18, v19, v18, vcc
	v_div_scale_f32 v19, s[14:15], v18, v18, 1.0
	v_rcp_f32_e32 v20, v19
	s_nop 0
	v_fma_f32 v21, -v19, v20, 1.0
	v_fmac_f32_e32 v20, v21, v20
	v_div_scale_f32 v21, vcc, 1.0, v18, 1.0
	v_mul_f32_e32 v22, v21, v20
	v_fma_f32 v23, -v19, v22, v21
	v_fmac_f32_e32 v22, v23, v20
	v_fma_f32 v19, -v19, v22, v21
	v_div_fmas_f32 v19, v19, v20, v22
	v_div_fixup_f32 v18, v19, v18, 1.0
	v_pk_mul_f32 v[36:37], v[36:37], v[18:19] op_sel_hi:[1,0]
	v_pk_mul_f32 v[38:39], v[38:39], v[18:19] op_sel_hi:[1,0]
	v_pk_mul_f32 v[40:41], v[40:41], v[18:19] op_sel_hi:[1,0]
	v_pk_mul_f32 v[42:43], v[42:43], v[18:19] op_sel_hi:[1,0]
	v_pk_mul_f32 v[36:37], v[36:37], v[100:101]
	v_pk_mul_f32 v[38:39], v[38:39], v[102:103]
	v_pk_mul_f32 v[40:41], v[40:41], v[104:105]
	v_pk_mul_f32 v[42:43], v[42:43], v[106:107]
	global_store_dwordx4 v[6:7], v[36:39], off
	global_store_dwordx4 v[6:7], v[40:43], off offset:16
	v_lshl_add_u64 v[6:7], v[6:7], 0, s[30:31]
	global_load_dwordx4 v[36:39], v[32:33], off
	global_load_dwordx4 v[40:43], v[32:33], off offset:16
	global_load_dword v44, v[26:27], off
	v_lshl_add_u64 v[32:33], v[32:33], 0, s[30:31]
	v_lshl_add_u64 v[26:27], v[26:27], 0, s[28:29]
	s_waitcnt vmcnt(3)
	s_nop 1
	v_add_f32_dpp v19, v45, v45 quad_perm:[1,0,3,2] row_mask:0xf bank_mask:0xf
	s_nop 1
	v_add_f32_dpp v18, v19, v19 quad_perm:[2,3,0,1] row_mask:0xf bank_mask:0xf
	s_nop 1
	v_add_f32_dpp v18, v18, v18 row_half_mirror row_mask:0xf bank_mask:0xf
	v_fmamk_f32 v18, v18, 0x39800000, v173
	v_mul_f32_e32 v19, 0x4f800000, v18
	v_cmp_gt_f32_e32 vcc, s51, v18
	s_nop 1
	v_cndmask_b32_e32 v18, v18, v19, vcc
	v_sqrt_f32_e32 v19, v18
	s_nop 0
	v_add_u32_e32 v20, -1, v19
	v_fma_f32 v22, -v20, v19, v18
	v_add_u32_e32 v21, 1, v19
	v_cmp_ge_f32_e64 s[14:15], 0, v22
	s_nop 1
	v_cndmask_b32_e64 v20, v19, v20, s[14:15]
	v_fma_f32 v19, -v21, v19, v18
	v_cmp_lt_f32_e64 s[14:15], 0, v19
	s_nop 1
	v_cndmask_b32_e64 v19, v20, v21, s[14:15]
	v_mul_f32_e32 v20, 0x37800000, v19
	v_cndmask_b32_e32 v19, v19, v20, vcc
	v_cmp_class_f32_e32 vcc, v18, v174
	s_nop 1
	v_cndmask_b32_e32 v18, v19, v18, vcc
	v_div_scale_f32 v19, s[14:15], v18, v18, 1.0
	v_rcp_f32_e32 v20, v19
	s_nop 0
	v_fma_f32 v21, -v19, v20, 1.0
	v_fmac_f32_e32 v20, v21, v20
	v_div_scale_f32 v21, vcc, 1.0, v18, 1.0
	v_mul_f32_e32 v22, v21, v20
	v_fma_f32 v23, -v19, v22, v21
	v_fmac_f32_e32 v22, v23, v20
	v_fma_f32 v19, -v19, v22, v21
	v_div_fmas_f32 v19, v19, v20, v22
	v_div_fixup_f32 v18, v19, v18, 1.0
	v_pk_mul_f32 v[10:11], v[10:11], v[18:19] op_sel_hi:[1,0]
	v_pk_mul_f32 v[12:13], v[12:13], v[18:19] op_sel_hi:[1,0]
	v_pk_mul_f32 v[14:15], v[14:15], v[18:19] op_sel_hi:[1,0]
	v_pk_mul_f32 v[16:17], v[16:17], v[18:19] op_sel_hi:[1,0]
	v_pk_mul_f32 v[10:11], v[10:11], v[100:101]
	v_pk_mul_f32 v[12:13], v[12:13], v[102:103]
	v_pk_mul_f32 v[14:15], v[14:15], v[104:105]
	v_pk_mul_f32 v[16:17], v[16:17], v[106:107]
	global_store_dwordx4 v[6:7], v[10:13], off
	global_store_dwordx4 v[6:7], v[14:17], off offset:16
	v_lshl_add_u64 v[6:7], v[6:7], 0, s[30:31]
	global_load_dwordx4 v[10:13], v[32:33], off
	global_load_dwordx4 v[14:17], v[32:33], off offset:16
	global_load_dword v45, v[26:27], off
	v_lshl_add_u64 v[32:33], v[32:33], 0, s[30:31]
	v_lshl_add_u64 v[26:27], v[26:27], 0, s[28:29]
	s_waitcnt vmcnt(3)
	s_nop 1
	v_add_f32_dpp v19, v44, v44 quad_perm:[1,0,3,2] row_mask:0xf bank_mask:0xf
	s_nop 1
	v_add_f32_dpp v18, v19, v19 quad_perm:[2,3,0,1] row_mask:0xf bank_mask:0xf
	s_nop 1
	v_add_f32_dpp v18, v18, v18 row_half_mirror row_mask:0xf bank_mask:0xf
	v_fmamk_f32 v18, v18, 0x39800000, v173
	v_mul_f32_e32 v19, 0x4f800000, v18
	v_cmp_gt_f32_e32 vcc, s51, v18
	s_nop 1
	v_cndmask_b32_e32 v18, v18, v19, vcc
	v_sqrt_f32_e32 v19, v18
	s_nop 0
	v_add_u32_e32 v20, -1, v19
	v_fma_f32 v22, -v20, v19, v18
	v_add_u32_e32 v21, 1, v19
	v_cmp_ge_f32_e64 s[14:15], 0, v22
	s_nop 1
	v_cndmask_b32_e64 v20, v19, v20, s[14:15]
	v_fma_f32 v19, -v21, v19, v18
	v_cmp_lt_f32_e64 s[14:15], 0, v19
	s_nop 1
	v_cndmask_b32_e64 v19, v20, v21, s[14:15]
	v_mul_f32_e32 v20, 0x37800000, v19
	v_cndmask_b32_e32 v19, v19, v20, vcc
	v_cmp_class_f32_e32 vcc, v18, v174
	s_nop 1
	v_cndmask_b32_e32 v18, v19, v18, vcc
	v_div_scale_f32 v19, s[14:15], v18, v18, 1.0
	v_rcp_f32_e32 v20, v19
	s_nop 0
	v_fma_f32 v21, -v19, v20, 1.0
	v_fmac_f32_e32 v20, v21, v20
	v_div_scale_f32 v21, vcc, 1.0, v18, 1.0
	v_mul_f32_e32 v22, v21, v20
	v_fma_f32 v23, -v19, v22, v21
	v_fmac_f32_e32 v22, v23, v20
	v_fma_f32 v19, -v19, v22, v21
	v_div_fmas_f32 v19, v19, v20, v22
	v_div_fixup_f32 v18, v19, v18, 1.0
	v_pk_mul_f32 v[36:37], v[36:37], v[18:19] op_sel_hi:[1,0]
	v_pk_mul_f32 v[38:39], v[38:39], v[18:19] op_sel_hi:[1,0]
	v_pk_mul_f32 v[40:41], v[40:41], v[18:19] op_sel_hi:[1,0]
	v_pk_mul_f32 v[42:43], v[42:43], v[18:19] op_sel_hi:[1,0]
	v_pk_mul_f32 v[36:37], v[36:37], v[100:101]
	v_pk_mul_f32 v[38:39], v[38:39], v[102:103]
	v_pk_mul_f32 v[40:41], v[40:41], v[104:105]
	v_pk_mul_f32 v[42:43], v[42:43], v[106:107]
	global_store_dwordx4 v[6:7], v[36:39], off
	global_store_dwordx4 v[6:7], v[40:43], off offset:16
	v_lshl_add_u64 v[6:7], v[6:7], 0, s[30:31]
	global_load_dwordx4 v[36:39], v[32:33], off
	global_load_dwordx4 v[40:43], v[32:33], off offset:16
	global_load_dword v44, v[26:27], off
	v_lshl_add_u64 v[32:33], v[32:33], 0, s[30:31]
	v_lshl_add_u64 v[26:27], v[26:27], 0, s[28:29]
	s_waitcnt vmcnt(3)
	s_nop 1
	v_add_f32_dpp v19, v45, v45 quad_perm:[1,0,3,2] row_mask:0xf bank_mask:0xf
	s_nop 1
	v_add_f32_dpp v18, v19, v19 quad_perm:[2,3,0,1] row_mask:0xf bank_mask:0xf
	s_nop 1
	v_add_f32_dpp v18, v18, v18 row_half_mirror row_mask:0xf bank_mask:0xf
	v_fmamk_f32 v18, v18, 0x39800000, v173
	v_mul_f32_e32 v19, 0x4f800000, v18
	v_cmp_gt_f32_e32 vcc, s51, v18
	s_nop 1
	v_cndmask_b32_e32 v18, v18, v19, vcc
	v_sqrt_f32_e32 v19, v18
	s_nop 0
	v_add_u32_e32 v20, -1, v19
	v_fma_f32 v22, -v20, v19, v18
	v_add_u32_e32 v21, 1, v19
	v_cmp_ge_f32_e64 s[14:15], 0, v22
	s_nop 1
	v_cndmask_b32_e64 v20, v19, v20, s[14:15]
	v_fma_f32 v19, -v21, v19, v18
	v_cmp_lt_f32_e64 s[14:15], 0, v19
	s_nop 1
	v_cndmask_b32_e64 v19, v20, v21, s[14:15]
	v_mul_f32_e32 v20, 0x37800000, v19
	v_cndmask_b32_e32 v19, v19, v20, vcc
	v_cmp_class_f32_e32 vcc, v18, v174
	s_nop 1
	v_cndmask_b32_e32 v18, v19, v18, vcc
	v_div_scale_f32 v19, s[14:15], v18, v18, 1.0
	v_rcp_f32_e32 v20, v19
	s_nop 0
	v_fma_f32 v21, -v19, v20, 1.0
	v_fmac_f32_e32 v20, v21, v20
	v_div_scale_f32 v21, vcc, 1.0, v18, 1.0
	v_mul_f32_e32 v22, v21, v20
	v_fma_f32 v23, -v19, v22, v21
	v_fmac_f32_e32 v22, v23, v20
	v_fma_f32 v19, -v19, v22, v21
	v_div_fmas_f32 v19, v19, v20, v22
	v_div_fixup_f32 v18, v19, v18, 1.0
	v_pk_mul_f32 v[10:11], v[10:11], v[18:19] op_sel_hi:[1,0]
	v_pk_mul_f32 v[12:13], v[12:13], v[18:19] op_sel_hi:[1,0]
	v_pk_mul_f32 v[14:15], v[14:15], v[18:19] op_sel_hi:[1,0]
	v_pk_mul_f32 v[16:17], v[16:17], v[18:19] op_sel_hi:[1,0]
	v_pk_mul_f32 v[10:11], v[10:11], v[100:101]
	v_pk_mul_f32 v[12:13], v[12:13], v[102:103]
	v_pk_mul_f32 v[14:15], v[14:15], v[104:105]
	v_pk_mul_f32 v[16:17], v[16:17], v[106:107]
	global_store_dwordx4 v[6:7], v[10:13], off
	global_store_dwordx4 v[6:7], v[14:17], off offset:16
	v_lshl_add_u64 v[6:7], v[6:7], 0, s[30:31]
	global_load_dwordx4 v[10:13], v[32:33], off
	global_load_dwordx4 v[14:17], v[32:33], off offset:16
	global_load_dword v45, v[26:27], off
	v_lshl_add_u64 v[32:33], v[32:33], 0, s[30:31]
	v_lshl_add_u64 v[26:27], v[26:27], 0, s[28:29]
	s_waitcnt vmcnt(3)
	s_nop 1
	v_add_f32_dpp v19, v44, v44 quad_perm:[1,0,3,2] row_mask:0xf bank_mask:0xf
	s_nop 1
	v_add_f32_dpp v18, v19, v19 quad_perm:[2,3,0,1] row_mask:0xf bank_mask:0xf
	s_nop 1
	v_add_f32_dpp v18, v18, v18 row_half_mirror row_mask:0xf bank_mask:0xf
	v_fmamk_f32 v18, v18, 0x39800000, v173
	v_mul_f32_e32 v19, 0x4f800000, v18
	v_cmp_gt_f32_e32 vcc, s51, v18
	s_nop 1
	v_cndmask_b32_e32 v18, v18, v19, vcc
	v_sqrt_f32_e32 v19, v18
	s_nop 0
	v_add_u32_e32 v20, -1, v19
	v_fma_f32 v22, -v20, v19, v18
	v_add_u32_e32 v21, 1, v19
	v_cmp_ge_f32_e64 s[14:15], 0, v22
	s_nop 1
	v_cndmask_b32_e64 v20, v19, v20, s[14:15]
	v_fma_f32 v19, -v21, v19, v18
	v_cmp_lt_f32_e64 s[14:15], 0, v19
	s_nop 1
	v_cndmask_b32_e64 v19, v20, v21, s[14:15]
	v_mul_f32_e32 v20, 0x37800000, v19
	v_cndmask_b32_e32 v19, v19, v20, vcc
	v_cmp_class_f32_e32 vcc, v18, v174
	s_nop 1
	v_cndmask_b32_e32 v18, v19, v18, vcc
	v_div_scale_f32 v19, s[14:15], v18, v18, 1.0
	v_rcp_f32_e32 v20, v19
	s_nop 0
	v_fma_f32 v21, -v19, v20, 1.0
	v_fmac_f32_e32 v20, v21, v20
	v_div_scale_f32 v21, vcc, 1.0, v18, 1.0
	v_mul_f32_e32 v22, v21, v20
	v_fma_f32 v23, -v19, v22, v21
	v_fmac_f32_e32 v22, v23, v20
	v_fma_f32 v19, -v19, v22, v21
	v_div_fmas_f32 v19, v19, v20, v22
	v_div_fixup_f32 v18, v19, v18, 1.0
	v_pk_mul_f32 v[36:37], v[36:37], v[18:19] op_sel_hi:[1,0]
	v_pk_mul_f32 v[38:39], v[38:39], v[18:19] op_sel_hi:[1,0]
	v_pk_mul_f32 v[40:41], v[40:41], v[18:19] op_sel_hi:[1,0]
	v_pk_mul_f32 v[42:43], v[42:43], v[18:19] op_sel_hi:[1,0]
	v_pk_mul_f32 v[36:37], v[36:37], v[100:101]
	v_pk_mul_f32 v[38:39], v[38:39], v[102:103]
	v_pk_mul_f32 v[40:41], v[40:41], v[104:105]
	v_pk_mul_f32 v[42:43], v[42:43], v[106:107]
	global_store_dwordx4 v[6:7], v[36:39], off
	global_store_dwordx4 v[6:7], v[40:43], off offset:16
	v_lshl_add_u64 v[6:7], v[6:7], 0, s[30:31]
	global_load_dwordx4 v[36:39], v[32:33], off
	global_load_dwordx4 v[40:43], v[32:33], off offset:16
	global_load_dword v44, v[26:27], off
	v_lshl_add_u64 v[32:33], v[32:33], 0, s[30:31]
	v_lshl_add_u64 v[26:27], v[26:27], 0, s[28:29]
	s_waitcnt vmcnt(3)
	s_nop 1
	v_add_f32_dpp v19, v45, v45 quad_perm:[1,0,3,2] row_mask:0xf bank_mask:0xf
	s_nop 1
	v_add_f32_dpp v18, v19, v19 quad_perm:[2,3,0,1] row_mask:0xf bank_mask:0xf
	s_nop 1
	v_add_f32_dpp v18, v18, v18 row_half_mirror row_mask:0xf bank_mask:0xf
	v_fmamk_f32 v18, v18, 0x39800000, v173
	v_mul_f32_e32 v19, 0x4f800000, v18
	v_cmp_gt_f32_e32 vcc, s51, v18
	s_nop 1
	v_cndmask_b32_e32 v18, v18, v19, vcc
	v_sqrt_f32_e32 v19, v18
	s_nop 0
	v_add_u32_e32 v20, -1, v19
	v_fma_f32 v22, -v20, v19, v18
	v_add_u32_e32 v21, 1, v19
	v_cmp_ge_f32_e64 s[14:15], 0, v22
	s_nop 1
	v_cndmask_b32_e64 v20, v19, v20, s[14:15]
	v_fma_f32 v19, -v21, v19, v18
	v_cmp_lt_f32_e64 s[14:15], 0, v19
	s_nop 1
	v_cndmask_b32_e64 v19, v20, v21, s[14:15]
	v_mul_f32_e32 v20, 0x37800000, v19
	v_cndmask_b32_e32 v19, v19, v20, vcc
	v_cmp_class_f32_e32 vcc, v18, v174
	s_nop 1
	v_cndmask_b32_e32 v18, v19, v18, vcc
	v_div_scale_f32 v19, s[14:15], v18, v18, 1.0
	v_rcp_f32_e32 v20, v19
	s_nop 0
	v_fma_f32 v21, -v19, v20, 1.0
	v_fmac_f32_e32 v20, v21, v20
	v_div_scale_f32 v21, vcc, 1.0, v18, 1.0
	v_mul_f32_e32 v22, v21, v20
	v_fma_f32 v23, -v19, v22, v21
	v_fmac_f32_e32 v22, v23, v20
	v_fma_f32 v19, -v19, v22, v21
	v_div_fmas_f32 v19, v19, v20, v22
	v_div_fixup_f32 v18, v19, v18, 1.0
	v_pk_mul_f32 v[10:11], v[10:11], v[18:19] op_sel_hi:[1,0]
	v_pk_mul_f32 v[12:13], v[12:13], v[18:19] op_sel_hi:[1,0]
	v_pk_mul_f32 v[14:15], v[14:15], v[18:19] op_sel_hi:[1,0]
	v_pk_mul_f32 v[16:17], v[16:17], v[18:19] op_sel_hi:[1,0]
	v_pk_mul_f32 v[10:11], v[10:11], v[100:101]
	v_pk_mul_f32 v[12:13], v[12:13], v[102:103]
	v_pk_mul_f32 v[14:15], v[14:15], v[104:105]
	v_pk_mul_f32 v[16:17], v[16:17], v[106:107]
	global_store_dwordx4 v[6:7], v[10:13], off
	global_store_dwordx4 v[6:7], v[14:17], off offset:16
	v_lshl_add_u64 v[6:7], v[6:7], 0, s[30:31]
	global_load_dwordx4 v[10:13], v[32:33], off
	global_load_dwordx4 v[14:17], v[32:33], off offset:16
	global_load_dword v45, v[26:27], off
	v_lshl_add_u64 v[32:33], v[32:33], 0, s[30:31]
	v_lshl_add_u64 v[26:27], v[26:27], 0, s[28:29]
	s_waitcnt vmcnt(3)
	s_nop 1
	v_add_f32_dpp v19, v44, v44 quad_perm:[1,0,3,2] row_mask:0xf bank_mask:0xf
	s_nop 1
	v_add_f32_dpp v18, v19, v19 quad_perm:[2,3,0,1] row_mask:0xf bank_mask:0xf
	s_nop 1
	v_add_f32_dpp v18, v18, v18 row_half_mirror row_mask:0xf bank_mask:0xf
	v_fmamk_f32 v18, v18, 0x39800000, v173
	v_mul_f32_e32 v19, 0x4f800000, v18
	v_cmp_gt_f32_e32 vcc, s51, v18
	s_nop 1
	v_cndmask_b32_e32 v18, v18, v19, vcc
	v_sqrt_f32_e32 v19, v18
	s_nop 0
	v_add_u32_e32 v20, -1, v19
	v_fma_f32 v22, -v20, v19, v18
	v_add_u32_e32 v21, 1, v19
	v_cmp_ge_f32_e64 s[14:15], 0, v22
	s_nop 1
	v_cndmask_b32_e64 v20, v19, v20, s[14:15]
	v_fma_f32 v19, -v21, v19, v18
	v_cmp_lt_f32_e64 s[14:15], 0, v19
	s_nop 1
	v_cndmask_b32_e64 v19, v20, v21, s[14:15]
	v_mul_f32_e32 v20, 0x37800000, v19
	v_cndmask_b32_e32 v19, v19, v20, vcc
	v_cmp_class_f32_e32 vcc, v18, v174
	s_nop 1
	v_cndmask_b32_e32 v18, v19, v18, vcc
	v_div_scale_f32 v19, s[14:15], v18, v18, 1.0
	v_rcp_f32_e32 v20, v19
	s_nop 0
	v_fma_f32 v21, -v19, v20, 1.0
	v_fmac_f32_e32 v20, v21, v20
	v_div_scale_f32 v21, vcc, 1.0, v18, 1.0
	v_mul_f32_e32 v22, v21, v20
	v_fma_f32 v23, -v19, v22, v21
	v_fmac_f32_e32 v22, v23, v20
	v_fma_f32 v19, -v19, v22, v21
	v_div_fmas_f32 v19, v19, v20, v22
	v_div_fixup_f32 v18, v19, v18, 1.0
	v_pk_mul_f32 v[36:37], v[36:37], v[18:19] op_sel_hi:[1,0]
	v_pk_mul_f32 v[38:39], v[38:39], v[18:19] op_sel_hi:[1,0]
	v_pk_mul_f32 v[40:41], v[40:41], v[18:19] op_sel_hi:[1,0]
	v_pk_mul_f32 v[42:43], v[42:43], v[18:19] op_sel_hi:[1,0]
	v_pk_mul_f32 v[36:37], v[36:37], v[100:101]
	v_pk_mul_f32 v[38:39], v[38:39], v[102:103]
	v_pk_mul_f32 v[40:41], v[40:41], v[104:105]
	v_pk_mul_f32 v[42:43], v[42:43], v[106:107]
	global_store_dwordx4 v[6:7], v[36:39], off
	global_store_dwordx4 v[6:7], v[40:43], off offset:16
	v_lshl_add_u64 v[6:7], v[6:7], 0, s[30:31]
	global_load_dwordx4 v[36:39], v[32:33], off
	global_load_dwordx4 v[40:43], v[32:33], off offset:16
	global_load_dword v44, v[26:27], off
	v_lshl_add_u64 v[32:33], v[32:33], 0, s[30:31]
	v_lshl_add_u64 v[26:27], v[26:27], 0, s[28:29]
	s_waitcnt vmcnt(3)
	s_nop 1
	v_add_f32_dpp v19, v45, v45 quad_perm:[1,0,3,2] row_mask:0xf bank_mask:0xf
	s_nop 1
	v_add_f32_dpp v18, v19, v19 quad_perm:[2,3,0,1] row_mask:0xf bank_mask:0xf
	s_nop 1
	v_add_f32_dpp v18, v18, v18 row_half_mirror row_mask:0xf bank_mask:0xf
	v_fmamk_f32 v18, v18, 0x39800000, v173
	v_mul_f32_e32 v19, 0x4f800000, v18
	v_cmp_gt_f32_e32 vcc, s51, v18
	s_nop 1
	v_cndmask_b32_e32 v18, v18, v19, vcc
	v_sqrt_f32_e32 v19, v18
	s_nop 0
	v_add_u32_e32 v20, -1, v19
	v_fma_f32 v22, -v20, v19, v18
	v_add_u32_e32 v21, 1, v19
	v_cmp_ge_f32_e64 s[14:15], 0, v22
	s_nop 1
	v_cndmask_b32_e64 v20, v19, v20, s[14:15]
	v_fma_f32 v19, -v21, v19, v18
	v_cmp_lt_f32_e64 s[14:15], 0, v19
	s_nop 1
	v_cndmask_b32_e64 v19, v20, v21, s[14:15]
	v_mul_f32_e32 v20, 0x37800000, v19
	v_cndmask_b32_e32 v19, v19, v20, vcc
	v_cmp_class_f32_e32 vcc, v18, v174
	s_nop 1
	v_cndmask_b32_e32 v18, v19, v18, vcc
	v_div_scale_f32 v19, s[14:15], v18, v18, 1.0
	v_rcp_f32_e32 v20, v19
	s_nop 0
	v_fma_f32 v21, -v19, v20, 1.0
	v_fmac_f32_e32 v20, v21, v20
	v_div_scale_f32 v21, vcc, 1.0, v18, 1.0
	v_mul_f32_e32 v22, v21, v20
	v_fma_f32 v23, -v19, v22, v21
	v_fmac_f32_e32 v22, v23, v20
	v_fma_f32 v19, -v19, v22, v21
	v_div_fmas_f32 v19, v19, v20, v22
	v_div_fixup_f32 v18, v19, v18, 1.0
	v_pk_mul_f32 v[10:11], v[10:11], v[18:19] op_sel_hi:[1,0]
	v_pk_mul_f32 v[12:13], v[12:13], v[18:19] op_sel_hi:[1,0]
	v_pk_mul_f32 v[14:15], v[14:15], v[18:19] op_sel_hi:[1,0]
	v_pk_mul_f32 v[16:17], v[16:17], v[18:19] op_sel_hi:[1,0]
	v_pk_mul_f32 v[10:11], v[10:11], v[100:101]
	v_pk_mul_f32 v[12:13], v[12:13], v[102:103]
	v_pk_mul_f32 v[14:15], v[14:15], v[104:105]
	v_pk_mul_f32 v[16:17], v[16:17], v[106:107]
	global_store_dwordx4 v[6:7], v[10:13], off
	global_store_dwordx4 v[6:7], v[14:17], off offset:16
	v_lshl_add_u64 v[6:7], v[6:7], 0, s[30:31]
	global_load_dwordx4 v[10:13], v[32:33], off
	global_load_dwordx4 v[14:17], v[32:33], off offset:16
	global_load_dword v45, v[26:27], off
	v_lshl_add_u64 v[32:33], v[32:33], 0, s[30:31]
	v_lshl_add_u64 v[26:27], v[26:27], 0, s[28:29]
	s_waitcnt vmcnt(3)
	s_nop 1
	v_add_f32_dpp v19, v44, v44 quad_perm:[1,0,3,2] row_mask:0xf bank_mask:0xf
	s_nop 1
	v_add_f32_dpp v18, v19, v19 quad_perm:[2,3,0,1] row_mask:0xf bank_mask:0xf
	s_nop 1
	v_add_f32_dpp v18, v18, v18 row_half_mirror row_mask:0xf bank_mask:0xf
	v_fmamk_f32 v18, v18, 0x39800000, v173
	v_mul_f32_e32 v19, 0x4f800000, v18
	v_cmp_gt_f32_e32 vcc, s51, v18
	s_nop 1
	v_cndmask_b32_e32 v18, v18, v19, vcc
	v_sqrt_f32_e32 v19, v18
	s_nop 0
	v_add_u32_e32 v20, -1, v19
	v_fma_f32 v22, -v20, v19, v18
	v_add_u32_e32 v21, 1, v19
	v_cmp_ge_f32_e64 s[14:15], 0, v22
	s_nop 1
	v_cndmask_b32_e64 v20, v19, v20, s[14:15]
	v_fma_f32 v19, -v21, v19, v18
	v_cmp_lt_f32_e64 s[14:15], 0, v19
	s_nop 1
	v_cndmask_b32_e64 v19, v20, v21, s[14:15]
	v_mul_f32_e32 v20, 0x37800000, v19
	v_cndmask_b32_e32 v19, v19, v20, vcc
	v_cmp_class_f32_e32 vcc, v18, v174
	s_nop 1
	v_cndmask_b32_e32 v18, v19, v18, vcc
	v_div_scale_f32 v19, s[14:15], v18, v18, 1.0
	v_rcp_f32_e32 v20, v19
	s_nop 0
	v_fma_f32 v21, -v19, v20, 1.0
	v_fmac_f32_e32 v20, v21, v20
	v_div_scale_f32 v21, vcc, 1.0, v18, 1.0
	v_mul_f32_e32 v22, v21, v20
	v_fma_f32 v23, -v19, v22, v21
	v_fmac_f32_e32 v22, v23, v20
	v_fma_f32 v19, -v19, v22, v21
	v_div_fmas_f32 v19, v19, v20, v22
	v_div_fixup_f32 v18, v19, v18, 1.0
	v_pk_mul_f32 v[36:37], v[36:37], v[18:19] op_sel_hi:[1,0]
	v_pk_mul_f32 v[38:39], v[38:39], v[18:19] op_sel_hi:[1,0]
	v_pk_mul_f32 v[40:41], v[40:41], v[18:19] op_sel_hi:[1,0]
	v_pk_mul_f32 v[42:43], v[42:43], v[18:19] op_sel_hi:[1,0]
	v_pk_mul_f32 v[36:37], v[36:37], v[100:101]
	v_pk_mul_f32 v[38:39], v[38:39], v[102:103]
	v_pk_mul_f32 v[40:41], v[40:41], v[104:105]
	v_pk_mul_f32 v[42:43], v[42:43], v[106:107]
	global_store_dwordx4 v[6:7], v[36:39], off
	global_store_dwordx4 v[6:7], v[40:43], off offset:16
	v_lshl_add_u64 v[6:7], v[6:7], 0, s[30:31]
	global_load_dwordx4 v[36:39], v[32:33], off
	global_load_dwordx4 v[40:43], v[32:33], off offset:16
	global_load_dword v44, v[26:27], off
	v_lshl_add_u64 v[32:33], v[32:33], 0, s[30:31]
	v_lshl_add_u64 v[26:27], v[26:27], 0, s[28:29]
	s_waitcnt vmcnt(3)
	s_nop 1
	v_add_f32_dpp v19, v45, v45 quad_perm:[1,0,3,2] row_mask:0xf bank_mask:0xf
	s_nop 1
	v_add_f32_dpp v18, v19, v19 quad_perm:[2,3,0,1] row_mask:0xf bank_mask:0xf
	s_nop 1
	v_add_f32_dpp v18, v18, v18 row_half_mirror row_mask:0xf bank_mask:0xf
	v_fmamk_f32 v18, v18, 0x39800000, v173
	v_mul_f32_e32 v19, 0x4f800000, v18
	v_cmp_gt_f32_e32 vcc, s51, v18
	s_nop 1
	v_cndmask_b32_e32 v18, v18, v19, vcc
	v_sqrt_f32_e32 v19, v18
	s_nop 0
	v_add_u32_e32 v20, -1, v19
	v_fma_f32 v22, -v20, v19, v18
	v_add_u32_e32 v21, 1, v19
	v_cmp_ge_f32_e64 s[14:15], 0, v22
	s_nop 1
	v_cndmask_b32_e64 v20, v19, v20, s[14:15]
	v_fma_f32 v19, -v21, v19, v18
	v_cmp_lt_f32_e64 s[14:15], 0, v19
	s_nop 1
	v_cndmask_b32_e64 v19, v20, v21, s[14:15]
	v_mul_f32_e32 v20, 0x37800000, v19
	v_cndmask_b32_e32 v19, v19, v20, vcc
	v_cmp_class_f32_e32 vcc, v18, v174
	s_nop 1
	v_cndmask_b32_e32 v18, v19, v18, vcc
	v_div_scale_f32 v19, s[14:15], v18, v18, 1.0
	v_rcp_f32_e32 v20, v19
	s_nop 0
	v_fma_f32 v21, -v19, v20, 1.0
	v_fmac_f32_e32 v20, v21, v20
	v_div_scale_f32 v21, vcc, 1.0, v18, 1.0
	v_mul_f32_e32 v22, v21, v20
	v_fma_f32 v23, -v19, v22, v21
	v_fmac_f32_e32 v22, v23, v20
	v_fma_f32 v19, -v19, v22, v21
	v_div_fmas_f32 v19, v19, v20, v22
	v_div_fixup_f32 v18, v19, v18, 1.0
	v_pk_mul_f32 v[10:11], v[10:11], v[18:19] op_sel_hi:[1,0]
	v_pk_mul_f32 v[12:13], v[12:13], v[18:19] op_sel_hi:[1,0]
	v_pk_mul_f32 v[14:15], v[14:15], v[18:19] op_sel_hi:[1,0]
	v_pk_mul_f32 v[16:17], v[16:17], v[18:19] op_sel_hi:[1,0]
	v_pk_mul_f32 v[10:11], v[10:11], v[100:101]
	v_pk_mul_f32 v[12:13], v[12:13], v[102:103]
	v_pk_mul_f32 v[14:15], v[14:15], v[104:105]
	v_pk_mul_f32 v[16:17], v[16:17], v[106:107]
	global_store_dwordx4 v[6:7], v[10:13], off
	global_store_dwordx4 v[6:7], v[14:17], off offset:16
	v_lshl_add_u64 v[6:7], v[6:7], 0, s[30:31]
	global_load_dwordx4 v[10:13], v[32:33], off
	global_load_dwordx4 v[14:17], v[32:33], off offset:16
	global_load_dword v45, v[26:27], off
	v_lshl_add_u64 v[32:33], v[32:33], 0, s[30:31]
	v_lshl_add_u64 v[26:27], v[26:27], 0, s[28:29]
	s_waitcnt vmcnt(3)
	s_nop 1
	v_add_f32_dpp v19, v44, v44 quad_perm:[1,0,3,2] row_mask:0xf bank_mask:0xf
	s_nop 1
	v_add_f32_dpp v18, v19, v19 quad_perm:[2,3,0,1] row_mask:0xf bank_mask:0xf
	s_nop 1
	v_add_f32_dpp v18, v18, v18 row_half_mirror row_mask:0xf bank_mask:0xf
	v_fmamk_f32 v18, v18, 0x39800000, v173
	v_mul_f32_e32 v19, 0x4f800000, v18
	v_cmp_gt_f32_e32 vcc, s51, v18
	s_nop 1
	v_cndmask_b32_e32 v18, v18, v19, vcc
	v_sqrt_f32_e32 v19, v18
	s_nop 0
	v_add_u32_e32 v20, -1, v19
	v_fma_f32 v22, -v20, v19, v18
	v_add_u32_e32 v21, 1, v19
	v_cmp_ge_f32_e64 s[14:15], 0, v22
	s_nop 1
	v_cndmask_b32_e64 v20, v19, v20, s[14:15]
	v_fma_f32 v19, -v21, v19, v18
	v_cmp_lt_f32_e64 s[14:15], 0, v19
	s_nop 1
	v_cndmask_b32_e64 v19, v20, v21, s[14:15]
	v_mul_f32_e32 v20, 0x37800000, v19
	v_cndmask_b32_e32 v19, v19, v20, vcc
	v_cmp_class_f32_e32 vcc, v18, v174
	s_nop 1
	v_cndmask_b32_e32 v18, v19, v18, vcc
	v_div_scale_f32 v19, s[14:15], v18, v18, 1.0
	v_rcp_f32_e32 v20, v19
	s_nop 0
	v_fma_f32 v21, -v19, v20, 1.0
	v_fmac_f32_e32 v20, v21, v20
	v_div_scale_f32 v21, vcc, 1.0, v18, 1.0
	v_mul_f32_e32 v22, v21, v20
	v_fma_f32 v23, -v19, v22, v21
	v_fmac_f32_e32 v22, v23, v20
	v_fma_f32 v19, -v19, v22, v21
	v_div_fmas_f32 v19, v19, v20, v22
	v_div_fixup_f32 v18, v19, v18, 1.0
	v_pk_mul_f32 v[36:37], v[36:37], v[18:19] op_sel_hi:[1,0]
	v_pk_mul_f32 v[38:39], v[38:39], v[18:19] op_sel_hi:[1,0]
	v_pk_mul_f32 v[40:41], v[40:41], v[18:19] op_sel_hi:[1,0]
	v_pk_mul_f32 v[42:43], v[42:43], v[18:19] op_sel_hi:[1,0]
	v_pk_mul_f32 v[36:37], v[36:37], v[100:101]
	v_pk_mul_f32 v[38:39], v[38:39], v[102:103]
	v_pk_mul_f32 v[40:41], v[40:41], v[104:105]
	v_pk_mul_f32 v[42:43], v[42:43], v[106:107]
	global_store_dwordx4 v[6:7], v[36:39], off
	global_store_dwordx4 v[6:7], v[40:43], off offset:16
	v_lshl_add_u64 v[6:7], v[6:7], 0, s[30:31]
	global_load_dwordx4 v[36:39], v[32:33], off
	global_load_dwordx4 v[40:43], v[32:33], off offset:16
	global_load_dword v44, v[26:27], off
	v_lshl_add_u64 v[32:33], v[32:33], 0, s[30:31]
	v_lshl_add_u64 v[26:27], v[26:27], 0, s[28:29]
	s_waitcnt vmcnt(3)
	s_nop 1
	v_add_f32_dpp v19, v45, v45 quad_perm:[1,0,3,2] row_mask:0xf bank_mask:0xf
	s_nop 1
	v_add_f32_dpp v18, v19, v19 quad_perm:[2,3,0,1] row_mask:0xf bank_mask:0xf
	s_nop 1
	v_add_f32_dpp v18, v18, v18 row_half_mirror row_mask:0xf bank_mask:0xf
	v_fmamk_f32 v18, v18, 0x39800000, v173
	v_mul_f32_e32 v19, 0x4f800000, v18
	v_cmp_gt_f32_e32 vcc, s51, v18
	s_nop 1
	v_cndmask_b32_e32 v18, v18, v19, vcc
	v_sqrt_f32_e32 v19, v18
	s_nop 0
	v_add_u32_e32 v20, -1, v19
	v_fma_f32 v22, -v20, v19, v18
	v_add_u32_e32 v21, 1, v19
	v_cmp_ge_f32_e64 s[14:15], 0, v22
	s_nop 1
	v_cndmask_b32_e64 v20, v19, v20, s[14:15]
	v_fma_f32 v19, -v21, v19, v18
	v_cmp_lt_f32_e64 s[14:15], 0, v19
	s_nop 1
	v_cndmask_b32_e64 v19, v20, v21, s[14:15]
	v_mul_f32_e32 v20, 0x37800000, v19
	v_cndmask_b32_e32 v19, v19, v20, vcc
	v_cmp_class_f32_e32 vcc, v18, v174
	s_nop 1
	v_cndmask_b32_e32 v18, v19, v18, vcc
	v_div_scale_f32 v19, s[14:15], v18, v18, 1.0
	v_rcp_f32_e32 v20, v19
	s_nop 0
	v_fma_f32 v21, -v19, v20, 1.0
	v_fmac_f32_e32 v20, v21, v20
	v_div_scale_f32 v21, vcc, 1.0, v18, 1.0
	v_mul_f32_e32 v22, v21, v20
	v_fma_f32 v23, -v19, v22, v21
	v_fmac_f32_e32 v22, v23, v20
	v_fma_f32 v19, -v19, v22, v21
	v_div_fmas_f32 v19, v19, v20, v22
	v_div_fixup_f32 v18, v19, v18, 1.0
	v_pk_mul_f32 v[10:11], v[10:11], v[18:19] op_sel_hi:[1,0]
	v_pk_mul_f32 v[12:13], v[12:13], v[18:19] op_sel_hi:[1,0]
	v_pk_mul_f32 v[14:15], v[14:15], v[18:19] op_sel_hi:[1,0]
	v_pk_mul_f32 v[16:17], v[16:17], v[18:19] op_sel_hi:[1,0]
	v_pk_mul_f32 v[10:11], v[10:11], v[100:101]
	v_pk_mul_f32 v[12:13], v[12:13], v[102:103]
	v_pk_mul_f32 v[14:15], v[14:15], v[104:105]
	v_pk_mul_f32 v[16:17], v[16:17], v[106:107]
	global_store_dwordx4 v[6:7], v[10:13], off
	global_store_dwordx4 v[6:7], v[14:17], off offset:16
	v_lshl_add_u64 v[6:7], v[6:7], 0, s[30:31]
	global_load_dwordx4 v[10:13], v[32:33], off
	global_load_dwordx4 v[14:17], v[32:33], off offset:16
	global_load_dword v45, v[26:27], off
	v_lshl_add_u64 v[32:33], v[32:33], 0, s[30:31]
	v_lshl_add_u64 v[26:27], v[26:27], 0, s[28:29]
	s_waitcnt vmcnt(3)
	s_nop 1
	v_add_f32_dpp v19, v44, v44 quad_perm:[1,0,3,2] row_mask:0xf bank_mask:0xf
	s_nop 1
	v_add_f32_dpp v18, v19, v19 quad_perm:[2,3,0,1] row_mask:0xf bank_mask:0xf
	s_nop 1
	v_add_f32_dpp v18, v18, v18 row_half_mirror row_mask:0xf bank_mask:0xf
	v_fmamk_f32 v18, v18, 0x39800000, v173
	v_mul_f32_e32 v19, 0x4f800000, v18
	v_cmp_gt_f32_e32 vcc, s51, v18
	s_nop 1
	v_cndmask_b32_e32 v18, v18, v19, vcc
	v_sqrt_f32_e32 v19, v18
	s_nop 0
	v_add_u32_e32 v20, -1, v19
	v_fma_f32 v22, -v20, v19, v18
	v_add_u32_e32 v21, 1, v19
	v_cmp_ge_f32_e64 s[14:15], 0, v22
	s_nop 1
	v_cndmask_b32_e64 v20, v19, v20, s[14:15]
	v_fma_f32 v19, -v21, v19, v18
	v_cmp_lt_f32_e64 s[14:15], 0, v19
	s_nop 1
	v_cndmask_b32_e64 v19, v20, v21, s[14:15]
	v_mul_f32_e32 v20, 0x37800000, v19
	v_cndmask_b32_e32 v19, v19, v20, vcc
	v_cmp_class_f32_e32 vcc, v18, v174
	s_nop 1
	v_cndmask_b32_e32 v18, v19, v18, vcc
	v_div_scale_f32 v19, s[14:15], v18, v18, 1.0
	v_rcp_f32_e32 v20, v19
	s_nop 0
	v_fma_f32 v21, -v19, v20, 1.0
	v_fmac_f32_e32 v20, v21, v20
	v_div_scale_f32 v21, vcc, 1.0, v18, 1.0
	v_mul_f32_e32 v22, v21, v20
	v_fma_f32 v23, -v19, v22, v21
	v_fmac_f32_e32 v22, v23, v20
	v_fma_f32 v19, -v19, v22, v21
	v_div_fmas_f32 v19, v19, v20, v22
	v_div_fixup_f32 v18, v19, v18, 1.0
	v_pk_mul_f32 v[36:37], v[36:37], v[18:19] op_sel_hi:[1,0]
	v_pk_mul_f32 v[38:39], v[38:39], v[18:19] op_sel_hi:[1,0]
	v_pk_mul_f32 v[40:41], v[40:41], v[18:19] op_sel_hi:[1,0]
	v_pk_mul_f32 v[42:43], v[42:43], v[18:19] op_sel_hi:[1,0]
	v_pk_mul_f32 v[36:37], v[36:37], v[100:101]
	v_pk_mul_f32 v[38:39], v[38:39], v[102:103]
	v_pk_mul_f32 v[40:41], v[40:41], v[104:105]
	v_pk_mul_f32 v[42:43], v[42:43], v[106:107]
	global_store_dwordx4 v[6:7], v[36:39], off
	global_store_dwordx4 v[6:7], v[40:43], off offset:16
	v_lshl_add_u64 v[6:7], v[6:7], 0, s[30:31]
	global_load_dwordx4 v[36:39], v[32:33], off
	global_load_dwordx4 v[40:43], v[32:33], off offset:16
	global_load_dword v44, v[26:27], off
	v_lshl_add_u64 v[32:33], v[32:33], 0, s[30:31]
	v_lshl_add_u64 v[26:27], v[26:27], 0, s[28:29]
	s_waitcnt vmcnt(3)
	s_nop 1
	v_add_f32_dpp v19, v45, v45 quad_perm:[1,0,3,2] row_mask:0xf bank_mask:0xf
	s_nop 1
	v_add_f32_dpp v18, v19, v19 quad_perm:[2,3,0,1] row_mask:0xf bank_mask:0xf
	s_nop 1
	v_add_f32_dpp v18, v18, v18 row_half_mirror row_mask:0xf bank_mask:0xf
	v_fmamk_f32 v18, v18, 0x39800000, v173
	v_mul_f32_e32 v19, 0x4f800000, v18
	v_cmp_gt_f32_e32 vcc, s51, v18
	s_nop 1
	v_cndmask_b32_e32 v18, v18, v19, vcc
	v_sqrt_f32_e32 v19, v18
	s_nop 0
	v_add_u32_e32 v20, -1, v19
	v_fma_f32 v22, -v20, v19, v18
	v_add_u32_e32 v21, 1, v19
	v_cmp_ge_f32_e64 s[14:15], 0, v22
	s_nop 1
	v_cndmask_b32_e64 v20, v19, v20, s[14:15]
	v_fma_f32 v19, -v21, v19, v18
	v_cmp_lt_f32_e64 s[14:15], 0, v19
	s_nop 1
	v_cndmask_b32_e64 v19, v20, v21, s[14:15]
	v_mul_f32_e32 v20, 0x37800000, v19
	v_cndmask_b32_e32 v19, v19, v20, vcc
	v_cmp_class_f32_e32 vcc, v18, v174
	s_nop 1
	v_cndmask_b32_e32 v18, v19, v18, vcc
	v_div_scale_f32 v19, s[14:15], v18, v18, 1.0
	v_rcp_f32_e32 v20, v19
	s_nop 0
	v_fma_f32 v21, -v19, v20, 1.0
	v_fmac_f32_e32 v20, v21, v20
	v_div_scale_f32 v21, vcc, 1.0, v18, 1.0
	v_mul_f32_e32 v22, v21, v20
	v_fma_f32 v23, -v19, v22, v21
	v_fmac_f32_e32 v22, v23, v20
	v_fma_f32 v19, -v19, v22, v21
	v_div_fmas_f32 v19, v19, v20, v22
	v_div_fixup_f32 v18, v19, v18, 1.0
	v_pk_mul_f32 v[10:11], v[10:11], v[18:19] op_sel_hi:[1,0]
	v_pk_mul_f32 v[12:13], v[12:13], v[18:19] op_sel_hi:[1,0]
	v_pk_mul_f32 v[14:15], v[14:15], v[18:19] op_sel_hi:[1,0]
	v_pk_mul_f32 v[16:17], v[16:17], v[18:19] op_sel_hi:[1,0]
	v_pk_mul_f32 v[10:11], v[10:11], v[100:101]
	v_pk_mul_f32 v[12:13], v[12:13], v[102:103]
	v_pk_mul_f32 v[14:15], v[14:15], v[104:105]
	v_pk_mul_f32 v[16:17], v[16:17], v[106:107]
	global_store_dwordx4 v[6:7], v[10:13], off
	global_store_dwordx4 v[6:7], v[14:17], off offset:16
	v_lshl_add_u64 v[6:7], v[6:7], 0, s[30:31]
	global_load_dwordx4 v[10:13], v[32:33], off
	global_load_dwordx4 v[14:17], v[32:33], off offset:16
	global_load_dword v45, v[26:27], off
	v_lshl_add_u64 v[32:33], v[32:33], 0, s[30:31]
	v_lshl_add_u64 v[26:27], v[26:27], 0, s[28:29]
	s_waitcnt vmcnt(3)
	s_nop 1
	v_add_f32_dpp v19, v44, v44 quad_perm:[1,0,3,2] row_mask:0xf bank_mask:0xf
	s_nop 1
	v_add_f32_dpp v18, v19, v19 quad_perm:[2,3,0,1] row_mask:0xf bank_mask:0xf
	s_nop 1
	v_add_f32_dpp v18, v18, v18 row_half_mirror row_mask:0xf bank_mask:0xf
	v_fmamk_f32 v18, v18, 0x39800000, v173
	v_mul_f32_e32 v19, 0x4f800000, v18
	v_cmp_gt_f32_e32 vcc, s51, v18
	s_nop 1
	v_cndmask_b32_e32 v18, v18, v19, vcc
	v_sqrt_f32_e32 v19, v18
	s_nop 0
	v_add_u32_e32 v20, -1, v19
	v_fma_f32 v22, -v20, v19, v18
	v_add_u32_e32 v21, 1, v19
	v_cmp_ge_f32_e64 s[14:15], 0, v22
	s_nop 1
	v_cndmask_b32_e64 v20, v19, v20, s[14:15]
	v_fma_f32 v19, -v21, v19, v18
	v_cmp_lt_f32_e64 s[14:15], 0, v19
	s_nop 1
	v_cndmask_b32_e64 v19, v20, v21, s[14:15]
	v_mul_f32_e32 v20, 0x37800000, v19
	v_cndmask_b32_e32 v19, v19, v20, vcc
	v_cmp_class_f32_e32 vcc, v18, v174
	s_nop 1
	v_cndmask_b32_e32 v18, v19, v18, vcc
	v_div_scale_f32 v19, s[14:15], v18, v18, 1.0
	v_rcp_f32_e32 v20, v19
	s_nop 0
	v_fma_f32 v21, -v19, v20, 1.0
	v_fmac_f32_e32 v20, v21, v20
	v_div_scale_f32 v21, vcc, 1.0, v18, 1.0
	v_mul_f32_e32 v22, v21, v20
	v_fma_f32 v23, -v19, v22, v21
	v_fmac_f32_e32 v22, v23, v20
	v_fma_f32 v19, -v19, v22, v21
	v_div_fmas_f32 v19, v19, v20, v22
	v_div_fixup_f32 v18, v19, v18, 1.0
	v_pk_mul_f32 v[36:37], v[36:37], v[18:19] op_sel_hi:[1,0]
	v_pk_mul_f32 v[38:39], v[38:39], v[18:19] op_sel_hi:[1,0]
	v_pk_mul_f32 v[40:41], v[40:41], v[18:19] op_sel_hi:[1,0]
	v_pk_mul_f32 v[42:43], v[42:43], v[18:19] op_sel_hi:[1,0]
	v_pk_mul_f32 v[36:37], v[36:37], v[100:101]
	v_pk_mul_f32 v[38:39], v[38:39], v[102:103]
	v_pk_mul_f32 v[40:41], v[40:41], v[104:105]
	v_pk_mul_f32 v[42:43], v[42:43], v[106:107]
	global_store_dwordx4 v[6:7], v[36:39], off
	global_store_dwordx4 v[6:7], v[40:43], off offset:16
	v_lshl_add_u64 v[6:7], v[6:7], 0, s[30:31]
	global_load_dwordx4 v[36:39], v[32:33], off
	global_load_dwordx4 v[40:43], v[32:33], off offset:16
	global_load_dword v44, v[26:27], off
	v_lshl_add_u64 v[32:33], v[32:33], 0, s[30:31]
	v_lshl_add_u64 v[26:27], v[26:27], 0, s[28:29]
	s_waitcnt vmcnt(3)
	s_nop 1
	v_add_f32_dpp v19, v45, v45 quad_perm:[1,0,3,2] row_mask:0xf bank_mask:0xf
	s_nop 1
	v_add_f32_dpp v18, v19, v19 quad_perm:[2,3,0,1] row_mask:0xf bank_mask:0xf
	s_nop 1
	v_add_f32_dpp v18, v18, v18 row_half_mirror row_mask:0xf bank_mask:0xf
	v_fmamk_f32 v18, v18, 0x39800000, v173
	v_mul_f32_e32 v19, 0x4f800000, v18
	v_cmp_gt_f32_e32 vcc, s51, v18
	s_nop 1
	v_cndmask_b32_e32 v18, v18, v19, vcc
	v_sqrt_f32_e32 v19, v18
	s_nop 0
	v_add_u32_e32 v20, -1, v19
	v_fma_f32 v22, -v20, v19, v18
	v_add_u32_e32 v21, 1, v19
	v_cmp_ge_f32_e64 s[14:15], 0, v22
	s_nop 1
	v_cndmask_b32_e64 v20, v19, v20, s[14:15]
	v_fma_f32 v19, -v21, v19, v18
	v_cmp_lt_f32_e64 s[14:15], 0, v19
	s_nop 1
	v_cndmask_b32_e64 v19, v20, v21, s[14:15]
	v_mul_f32_e32 v20, 0x37800000, v19
	v_cndmask_b32_e32 v19, v19, v20, vcc
	v_cmp_class_f32_e32 vcc, v18, v174
	s_nop 1
	v_cndmask_b32_e32 v18, v19, v18, vcc
	v_div_scale_f32 v19, s[14:15], v18, v18, 1.0
	v_rcp_f32_e32 v20, v19
	s_nop 0
	v_fma_f32 v21, -v19, v20, 1.0
	v_fmac_f32_e32 v20, v21, v20
	v_div_scale_f32 v21, vcc, 1.0, v18, 1.0
	v_mul_f32_e32 v22, v21, v20
	v_fma_f32 v23, -v19, v22, v21
	v_fmac_f32_e32 v22, v23, v20
	v_fma_f32 v19, -v19, v22, v21
	v_div_fmas_f32 v19, v19, v20, v22
	v_div_fixup_f32 v18, v19, v18, 1.0
	v_pk_mul_f32 v[10:11], v[10:11], v[18:19] op_sel_hi:[1,0]
	v_pk_mul_f32 v[12:13], v[12:13], v[18:19] op_sel_hi:[1,0]
	v_pk_mul_f32 v[14:15], v[14:15], v[18:19] op_sel_hi:[1,0]
	v_pk_mul_f32 v[16:17], v[16:17], v[18:19] op_sel_hi:[1,0]
	v_pk_mul_f32 v[10:11], v[10:11], v[100:101]
	v_pk_mul_f32 v[12:13], v[12:13], v[102:103]
	v_pk_mul_f32 v[14:15], v[14:15], v[104:105]
	v_pk_mul_f32 v[16:17], v[16:17], v[106:107]
	global_store_dwordx4 v[6:7], v[10:13], off
	global_store_dwordx4 v[6:7], v[14:17], off offset:16
	v_lshl_add_u64 v[6:7], v[6:7], 0, s[30:31]
	global_load_dwordx4 v[10:13], v[32:33], off
	global_load_dwordx4 v[14:17], v[32:33], off offset:16
	global_load_dword v45, v[26:27], off
	v_lshl_add_u64 v[32:33], v[32:33], 0, s[30:31]
	v_lshl_add_u64 v[26:27], v[26:27], 0, s[28:29]
	s_waitcnt vmcnt(3)
	s_nop 1
	v_add_f32_dpp v19, v44, v44 quad_perm:[1,0,3,2] row_mask:0xf bank_mask:0xf
	s_nop 1
	v_add_f32_dpp v18, v19, v19 quad_perm:[2,3,0,1] row_mask:0xf bank_mask:0xf
	s_nop 1
	v_add_f32_dpp v18, v18, v18 row_half_mirror row_mask:0xf bank_mask:0xf
	v_fmamk_f32 v18, v18, 0x39800000, v173
	v_mul_f32_e32 v19, 0x4f800000, v18
	v_cmp_gt_f32_e32 vcc, s51, v18
	s_nop 1
	v_cndmask_b32_e32 v18, v18, v19, vcc
	v_sqrt_f32_e32 v19, v18
	s_nop 0
	v_add_u32_e32 v20, -1, v19
	v_fma_f32 v22, -v20, v19, v18
	v_add_u32_e32 v21, 1, v19
	v_cmp_ge_f32_e64 s[14:15], 0, v22
	s_nop 1
	v_cndmask_b32_e64 v20, v19, v20, s[14:15]
	v_fma_f32 v19, -v21, v19, v18
	v_cmp_lt_f32_e64 s[14:15], 0, v19
	s_nop 1
	v_cndmask_b32_e64 v19, v20, v21, s[14:15]
	v_mul_f32_e32 v20, 0x37800000, v19
	v_cndmask_b32_e32 v19, v19, v20, vcc
	v_cmp_class_f32_e32 vcc, v18, v174
	s_nop 1
	v_cndmask_b32_e32 v18, v19, v18, vcc
	v_div_scale_f32 v19, s[14:15], v18, v18, 1.0
	v_rcp_f32_e32 v20, v19
	s_nop 0
	v_fma_f32 v21, -v19, v20, 1.0
	v_fmac_f32_e32 v20, v21, v20
	v_div_scale_f32 v21, vcc, 1.0, v18, 1.0
	v_mul_f32_e32 v22, v21, v20
	v_fma_f32 v23, -v19, v22, v21
	v_fmac_f32_e32 v22, v23, v20
	v_fma_f32 v19, -v19, v22, v21
	v_div_fmas_f32 v19, v19, v20, v22
	v_div_fixup_f32 v18, v19, v18, 1.0
	v_pk_mul_f32 v[36:37], v[36:37], v[18:19] op_sel_hi:[1,0]
	v_pk_mul_f32 v[38:39], v[38:39], v[18:19] op_sel_hi:[1,0]
	v_pk_mul_f32 v[40:41], v[40:41], v[18:19] op_sel_hi:[1,0]
	v_pk_mul_f32 v[42:43], v[42:43], v[18:19] op_sel_hi:[1,0]
	v_pk_mul_f32 v[36:37], v[36:37], v[100:101]
	v_pk_mul_f32 v[38:39], v[38:39], v[102:103]
	v_pk_mul_f32 v[40:41], v[40:41], v[104:105]
	v_pk_mul_f32 v[42:43], v[42:43], v[106:107]
	global_store_dwordx4 v[6:7], v[36:39], off
	global_store_dwordx4 v[6:7], v[40:43], off offset:16
	v_lshl_add_u64 v[6:7], v[6:7], 0, s[30:31]
	global_load_dwordx4 v[36:39], v[32:33], off
	global_load_dwordx4 v[40:43], v[32:33], off offset:16
	global_load_dword v44, v[26:27], off
	v_lshl_add_u64 v[32:33], v[32:33], 0, s[30:31]
	v_lshl_add_u64 v[26:27], v[26:27], 0, s[28:29]
	s_waitcnt vmcnt(3)
	s_nop 1
	v_add_f32_dpp v19, v45, v45 quad_perm:[1,0,3,2] row_mask:0xf bank_mask:0xf
	s_nop 1
	v_add_f32_dpp v18, v19, v19 quad_perm:[2,3,0,1] row_mask:0xf bank_mask:0xf
	s_nop 1
	v_add_f32_dpp v18, v18, v18 row_half_mirror row_mask:0xf bank_mask:0xf
	v_fmamk_f32 v18, v18, 0x39800000, v173
	v_mul_f32_e32 v19, 0x4f800000, v18
	v_cmp_gt_f32_e32 vcc, s51, v18
	s_nop 1
	v_cndmask_b32_e32 v18, v18, v19, vcc
	v_sqrt_f32_e32 v19, v18
	s_nop 0
	v_add_u32_e32 v20, -1, v19
	v_fma_f32 v22, -v20, v19, v18
	v_add_u32_e32 v21, 1, v19
	v_cmp_ge_f32_e64 s[14:15], 0, v22
	s_nop 1
	v_cndmask_b32_e64 v20, v19, v20, s[14:15]
	v_fma_f32 v19, -v21, v19, v18
	v_cmp_lt_f32_e64 s[14:15], 0, v19
	s_nop 1
	v_cndmask_b32_e64 v19, v20, v21, s[14:15]
	v_mul_f32_e32 v20, 0x37800000, v19
	v_cndmask_b32_e32 v19, v19, v20, vcc
	v_cmp_class_f32_e32 vcc, v18, v174
	s_nop 1
	v_cndmask_b32_e32 v18, v19, v18, vcc
	v_div_scale_f32 v19, s[14:15], v18, v18, 1.0
	v_rcp_f32_e32 v20, v19
	s_nop 0
	v_fma_f32 v21, -v19, v20, 1.0
	v_fmac_f32_e32 v20, v21, v20
	v_div_scale_f32 v21, vcc, 1.0, v18, 1.0
	v_mul_f32_e32 v22, v21, v20
	v_fma_f32 v23, -v19, v22, v21
	v_fmac_f32_e32 v22, v23, v20
	v_fma_f32 v19, -v19, v22, v21
	v_div_fmas_f32 v19, v19, v20, v22
	v_div_fixup_f32 v18, v19, v18, 1.0
	v_pk_mul_f32 v[10:11], v[10:11], v[18:19] op_sel_hi:[1,0]
	v_pk_mul_f32 v[12:13], v[12:13], v[18:19] op_sel_hi:[1,0]
	v_pk_mul_f32 v[14:15], v[14:15], v[18:19] op_sel_hi:[1,0]
	v_pk_mul_f32 v[16:17], v[16:17], v[18:19] op_sel_hi:[1,0]
	v_pk_mul_f32 v[10:11], v[10:11], v[100:101]
	v_pk_mul_f32 v[12:13], v[12:13], v[102:103]
	v_pk_mul_f32 v[14:15], v[14:15], v[104:105]
	v_pk_mul_f32 v[16:17], v[16:17], v[106:107]
	global_store_dwordx4 v[6:7], v[10:13], off
	global_store_dwordx4 v[6:7], v[14:17], off offset:16
	v_lshl_add_u64 v[6:7], v[6:7], 0, s[30:31]
	global_load_dwordx4 v[10:13], v[32:33], off
	global_load_dwordx4 v[14:17], v[32:33], off offset:16
	global_load_dword v45, v[26:27], off
	v_lshl_add_u64 v[32:33], v[32:33], 0, s[30:31]
	v_lshl_add_u64 v[26:27], v[26:27], 0, s[28:29]
	s_waitcnt vmcnt(3)
	s_nop 1
	v_add_f32_dpp v19, v44, v44 quad_perm:[1,0,3,2] row_mask:0xf bank_mask:0xf
	s_nop 1
	v_add_f32_dpp v18, v19, v19 quad_perm:[2,3,0,1] row_mask:0xf bank_mask:0xf
	s_nop 1
	v_add_f32_dpp v18, v18, v18 row_half_mirror row_mask:0xf bank_mask:0xf
	v_fmamk_f32 v18, v18, 0x39800000, v173
	v_mul_f32_e32 v19, 0x4f800000, v18
	v_cmp_gt_f32_e32 vcc, s51, v18
	s_nop 1
	v_cndmask_b32_e32 v18, v18, v19, vcc
	v_sqrt_f32_e32 v19, v18
	s_nop 0
	v_add_u32_e32 v20, -1, v19
	v_fma_f32 v22, -v20, v19, v18
	v_add_u32_e32 v21, 1, v19
	v_cmp_ge_f32_e64 s[14:15], 0, v22
	s_nop 1
	v_cndmask_b32_e64 v20, v19, v20, s[14:15]
	v_fma_f32 v19, -v21, v19, v18
	v_cmp_lt_f32_e64 s[14:15], 0, v19
	s_nop 1
	v_cndmask_b32_e64 v19, v20, v21, s[14:15]
	v_mul_f32_e32 v20, 0x37800000, v19
	v_cndmask_b32_e32 v19, v19, v20, vcc
	v_cmp_class_f32_e32 vcc, v18, v174
	s_nop 1
	v_cndmask_b32_e32 v18, v19, v18, vcc
	v_div_scale_f32 v19, s[14:15], v18, v18, 1.0
	v_rcp_f32_e32 v20, v19
	s_nop 0
	v_fma_f32 v21, -v19, v20, 1.0
	v_fmac_f32_e32 v20, v21, v20
	v_div_scale_f32 v21, vcc, 1.0, v18, 1.0
	v_mul_f32_e32 v22, v21, v20
	v_fma_f32 v23, -v19, v22, v21
	v_fmac_f32_e32 v22, v23, v20
	v_fma_f32 v19, -v19, v22, v21
	v_div_fmas_f32 v19, v19, v20, v22
	v_div_fixup_f32 v18, v19, v18, 1.0
	v_pk_mul_f32 v[36:37], v[36:37], v[18:19] op_sel_hi:[1,0]
	v_pk_mul_f32 v[38:39], v[38:39], v[18:19] op_sel_hi:[1,0]
	v_pk_mul_f32 v[40:41], v[40:41], v[18:19] op_sel_hi:[1,0]
	v_pk_mul_f32 v[42:43], v[42:43], v[18:19] op_sel_hi:[1,0]
	v_pk_mul_f32 v[36:37], v[36:37], v[100:101]
	v_pk_mul_f32 v[38:39], v[38:39], v[102:103]
	v_pk_mul_f32 v[40:41], v[40:41], v[104:105]
	v_pk_mul_f32 v[42:43], v[42:43], v[106:107]
	global_store_dwordx4 v[6:7], v[36:39], off
	global_store_dwordx4 v[6:7], v[40:43], off offset:16
	v_lshl_add_u64 v[6:7], v[6:7], 0, s[30:31]
	global_load_dwordx4 v[36:39], v[32:33], off
	global_load_dwordx4 v[40:43], v[32:33], off offset:16
	global_load_dword v44, v[26:27], off
	v_lshl_add_u64 v[32:33], v[32:33], 0, s[30:31]
	v_lshl_add_u64 v[26:27], v[26:27], 0, s[28:29]
	s_waitcnt vmcnt(3)
	s_nop 1
	v_add_f32_dpp v19, v45, v45 quad_perm:[1,0,3,2] row_mask:0xf bank_mask:0xf
	s_nop 1
	v_add_f32_dpp v18, v19, v19 quad_perm:[2,3,0,1] row_mask:0xf bank_mask:0xf
	s_nop 1
	v_add_f32_dpp v18, v18, v18 row_half_mirror row_mask:0xf bank_mask:0xf
	v_fmamk_f32 v18, v18, 0x39800000, v173
	v_mul_f32_e32 v19, 0x4f800000, v18
	v_cmp_gt_f32_e32 vcc, s51, v18
	s_nop 1
	v_cndmask_b32_e32 v18, v18, v19, vcc
	v_sqrt_f32_e32 v19, v18
	s_nop 0
	v_add_u32_e32 v20, -1, v19
	v_fma_f32 v22, -v20, v19, v18
	v_add_u32_e32 v21, 1, v19
	v_cmp_ge_f32_e64 s[14:15], 0, v22
	s_nop 1
	v_cndmask_b32_e64 v20, v19, v20, s[14:15]
	v_fma_f32 v19, -v21, v19, v18
	v_cmp_lt_f32_e64 s[14:15], 0, v19
	s_nop 1
	v_cndmask_b32_e64 v19, v20, v21, s[14:15]
	v_mul_f32_e32 v20, 0x37800000, v19
	v_cndmask_b32_e32 v19, v19, v20, vcc
	v_cmp_class_f32_e32 vcc, v18, v174
	s_nop 1
	v_cndmask_b32_e32 v18, v19, v18, vcc
	v_div_scale_f32 v19, s[14:15], v18, v18, 1.0
	v_rcp_f32_e32 v20, v19
	s_nop 0
	v_fma_f32 v21, -v19, v20, 1.0
	v_fmac_f32_e32 v20, v21, v20
	v_div_scale_f32 v21, vcc, 1.0, v18, 1.0
	v_mul_f32_e32 v22, v21, v20
	v_fma_f32 v23, -v19, v22, v21
	v_fmac_f32_e32 v22, v23, v20
	v_fma_f32 v19, -v19, v22, v21
	v_div_fmas_f32 v19, v19, v20, v22
	v_div_fixup_f32 v18, v19, v18, 1.0
	v_pk_mul_f32 v[10:11], v[10:11], v[18:19] op_sel_hi:[1,0]
	v_pk_mul_f32 v[12:13], v[12:13], v[18:19] op_sel_hi:[1,0]
	v_pk_mul_f32 v[14:15], v[14:15], v[18:19] op_sel_hi:[1,0]
	v_pk_mul_f32 v[16:17], v[16:17], v[18:19] op_sel_hi:[1,0]
	v_pk_mul_f32 v[10:11], v[10:11], v[100:101]
	v_pk_mul_f32 v[12:13], v[12:13], v[102:103]
	v_pk_mul_f32 v[14:15], v[14:15], v[104:105]
	v_pk_mul_f32 v[16:17], v[16:17], v[106:107]
	global_store_dwordx4 v[6:7], v[10:13], off
	global_store_dwordx4 v[6:7], v[14:17], off offset:16
	v_lshl_add_u64 v[6:7], v[6:7], 0, s[30:31]
	global_load_dwordx4 v[10:13], v[32:33], off
	global_load_dwordx4 v[14:17], v[32:33], off offset:16
	global_load_dword v45, v[26:27], off
	v_lshl_add_u64 v[32:33], v[32:33], 0, s[30:31]
	v_lshl_add_u64 v[26:27], v[26:27], 0, s[28:29]
	s_waitcnt vmcnt(3)
	s_nop 1
	v_add_f32_dpp v19, v44, v44 quad_perm:[1,0,3,2] row_mask:0xf bank_mask:0xf
	s_nop 1
	v_add_f32_dpp v18, v19, v19 quad_perm:[2,3,0,1] row_mask:0xf bank_mask:0xf
	s_nop 1
	v_add_f32_dpp v18, v18, v18 row_half_mirror row_mask:0xf bank_mask:0xf
	v_fmamk_f32 v18, v18, 0x39800000, v173
	v_mul_f32_e32 v19, 0x4f800000, v18
	v_cmp_gt_f32_e32 vcc, s51, v18
	s_nop 1
	v_cndmask_b32_e32 v18, v18, v19, vcc
	v_sqrt_f32_e32 v19, v18
	s_nop 0
	v_add_u32_e32 v20, -1, v19
	v_fma_f32 v22, -v20, v19, v18
	v_add_u32_e32 v21, 1, v19
	v_cmp_ge_f32_e64 s[14:15], 0, v22
	s_nop 1
	v_cndmask_b32_e64 v20, v19, v20, s[14:15]
	v_fma_f32 v19, -v21, v19, v18
	v_cmp_lt_f32_e64 s[14:15], 0, v19
	s_nop 1
	v_cndmask_b32_e64 v19, v20, v21, s[14:15]
	v_mul_f32_e32 v20, 0x37800000, v19
	v_cndmask_b32_e32 v19, v19, v20, vcc
	v_cmp_class_f32_e32 vcc, v18, v174
	s_nop 1
	v_cndmask_b32_e32 v18, v19, v18, vcc
	v_div_scale_f32 v19, s[14:15], v18, v18, 1.0
	v_rcp_f32_e32 v20, v19
	s_nop 0
	v_fma_f32 v21, -v19, v20, 1.0
	v_fmac_f32_e32 v20, v21, v20
	v_div_scale_f32 v21, vcc, 1.0, v18, 1.0
	v_mul_f32_e32 v22, v21, v20
	v_fma_f32 v23, -v19, v22, v21
	v_fmac_f32_e32 v22, v23, v20
	v_fma_f32 v19, -v19, v22, v21
	v_div_fmas_f32 v19, v19, v20, v22
	v_div_fixup_f32 v18, v19, v18, 1.0
	v_pk_mul_f32 v[36:37], v[36:37], v[18:19] op_sel_hi:[1,0]
	v_pk_mul_f32 v[38:39], v[38:39], v[18:19] op_sel_hi:[1,0]
	v_pk_mul_f32 v[40:41], v[40:41], v[18:19] op_sel_hi:[1,0]
	v_pk_mul_f32 v[42:43], v[42:43], v[18:19] op_sel_hi:[1,0]
	v_pk_mul_f32 v[36:37], v[36:37], v[100:101]
	v_pk_mul_f32 v[38:39], v[38:39], v[102:103]
	v_pk_mul_f32 v[40:41], v[40:41], v[104:105]
	v_pk_mul_f32 v[42:43], v[42:43], v[106:107]
	global_store_dwordx4 v[6:7], v[36:39], off
	global_store_dwordx4 v[6:7], v[40:43], off offset:16
	v_lshl_add_u64 v[6:7], v[6:7], 0, s[30:31]
	global_load_dwordx4 v[36:39], v[32:33], off
	global_load_dwordx4 v[40:43], v[32:33], off offset:16
	global_load_dword v44, v[26:27], off
	v_lshl_add_u64 v[32:33], v[32:33], 0, s[30:31]
	v_lshl_add_u64 v[26:27], v[26:27], 0, s[28:29]
	s_waitcnt vmcnt(3)
	s_nop 1
	v_add_f32_dpp v19, v45, v45 quad_perm:[1,0,3,2] row_mask:0xf bank_mask:0xf
	s_nop 1
	v_add_f32_dpp v18, v19, v19 quad_perm:[2,3,0,1] row_mask:0xf bank_mask:0xf
	s_nop 1
	v_add_f32_dpp v18, v18, v18 row_half_mirror row_mask:0xf bank_mask:0xf
	v_fmamk_f32 v18, v18, 0x39800000, v173
	v_mul_f32_e32 v19, 0x4f800000, v18
	v_cmp_gt_f32_e32 vcc, s51, v18
	s_nop 1
	v_cndmask_b32_e32 v18, v18, v19, vcc
	v_sqrt_f32_e32 v19, v18
	s_nop 0
	v_add_u32_e32 v20, -1, v19
	v_fma_f32 v22, -v20, v19, v18
	v_add_u32_e32 v21, 1, v19
	v_cmp_ge_f32_e64 s[14:15], 0, v22
	s_nop 1
	v_cndmask_b32_e64 v20, v19, v20, s[14:15]
	v_fma_f32 v19, -v21, v19, v18
	v_cmp_lt_f32_e64 s[14:15], 0, v19
	s_nop 1
	v_cndmask_b32_e64 v19, v20, v21, s[14:15]
	v_mul_f32_e32 v20, 0x37800000, v19
	v_cndmask_b32_e32 v19, v19, v20, vcc
	v_cmp_class_f32_e32 vcc, v18, v174
	s_nop 1
	v_cndmask_b32_e32 v18, v19, v18, vcc
	v_div_scale_f32 v19, s[14:15], v18, v18, 1.0
	v_rcp_f32_e32 v20, v19
	s_nop 0
	v_fma_f32 v21, -v19, v20, 1.0
	v_fmac_f32_e32 v20, v21, v20
	v_div_scale_f32 v21, vcc, 1.0, v18, 1.0
	v_mul_f32_e32 v22, v21, v20
	v_fma_f32 v23, -v19, v22, v21
	v_fmac_f32_e32 v22, v23, v20
	v_fma_f32 v19, -v19, v22, v21
	v_div_fmas_f32 v19, v19, v20, v22
	v_div_fixup_f32 v18, v19, v18, 1.0
	v_pk_mul_f32 v[10:11], v[10:11], v[18:19] op_sel_hi:[1,0]
	v_pk_mul_f32 v[12:13], v[12:13], v[18:19] op_sel_hi:[1,0]
	v_pk_mul_f32 v[14:15], v[14:15], v[18:19] op_sel_hi:[1,0]
	v_pk_mul_f32 v[16:17], v[16:17], v[18:19] op_sel_hi:[1,0]
	v_pk_mul_f32 v[10:11], v[10:11], v[100:101]
	v_pk_mul_f32 v[12:13], v[12:13], v[102:103]
	v_pk_mul_f32 v[14:15], v[14:15], v[104:105]
	v_pk_mul_f32 v[16:17], v[16:17], v[106:107]
	global_store_dwordx4 v[6:7], v[10:13], off
	global_store_dwordx4 v[6:7], v[14:17], off offset:16
	v_lshl_add_u64 v[6:7], v[6:7], 0, s[30:31]
	global_load_dwordx4 v[10:13], v[32:33], off
	global_load_dwordx4 v[14:17], v[32:33], off offset:16
	global_load_dword v45, v[26:27], off
	v_lshl_add_u64 v[32:33], v[32:33], 0, s[30:31]
	v_lshl_add_u64 v[26:27], v[26:27], 0, s[28:29]
	s_waitcnt vmcnt(3)
	s_nop 1
	v_add_f32_dpp v19, v44, v44 quad_perm:[1,0,3,2] row_mask:0xf bank_mask:0xf
	s_nop 1
	v_add_f32_dpp v18, v19, v19 quad_perm:[2,3,0,1] row_mask:0xf bank_mask:0xf
	s_nop 1
	v_add_f32_dpp v18, v18, v18 row_half_mirror row_mask:0xf bank_mask:0xf
	v_fmamk_f32 v18, v18, 0x39800000, v173
	v_mul_f32_e32 v19, 0x4f800000, v18
	v_cmp_gt_f32_e32 vcc, s51, v18
	s_nop 1
	v_cndmask_b32_e32 v18, v18, v19, vcc
	v_sqrt_f32_e32 v19, v18
	s_nop 0
	v_add_u32_e32 v20, -1, v19
	v_fma_f32 v22, -v20, v19, v18
	v_add_u32_e32 v21, 1, v19
	v_cmp_ge_f32_e64 s[14:15], 0, v22
	s_nop 1
	v_cndmask_b32_e64 v20, v19, v20, s[14:15]
	v_fma_f32 v19, -v21, v19, v18
	v_cmp_lt_f32_e64 s[14:15], 0, v19
	s_nop 1
	v_cndmask_b32_e64 v19, v20, v21, s[14:15]
	v_mul_f32_e32 v20, 0x37800000, v19
	v_cndmask_b32_e32 v19, v19, v20, vcc
	v_cmp_class_f32_e32 vcc, v18, v174
	s_nop 1
	v_cndmask_b32_e32 v18, v19, v18, vcc
	v_div_scale_f32 v19, s[14:15], v18, v18, 1.0
	v_rcp_f32_e32 v20, v19
	s_nop 0
	v_fma_f32 v21, -v19, v20, 1.0
	v_fmac_f32_e32 v20, v21, v20
	v_div_scale_f32 v21, vcc, 1.0, v18, 1.0
	v_mul_f32_e32 v22, v21, v20
	v_fma_f32 v23, -v19, v22, v21
	v_fmac_f32_e32 v22, v23, v20
	v_fma_f32 v19, -v19, v22, v21
	v_div_fmas_f32 v19, v19, v20, v22
	v_div_fixup_f32 v18, v19, v18, 1.0
	v_pk_mul_f32 v[36:37], v[36:37], v[18:19] op_sel_hi:[1,0]
	v_pk_mul_f32 v[38:39], v[38:39], v[18:19] op_sel_hi:[1,0]
	v_pk_mul_f32 v[40:41], v[40:41], v[18:19] op_sel_hi:[1,0]
	v_pk_mul_f32 v[42:43], v[42:43], v[18:19] op_sel_hi:[1,0]
	v_pk_mul_f32 v[36:37], v[36:37], v[100:101]
	v_pk_mul_f32 v[38:39], v[38:39], v[102:103]
	v_pk_mul_f32 v[40:41], v[40:41], v[104:105]
	v_pk_mul_f32 v[42:43], v[42:43], v[106:107]
	global_store_dwordx4 v[6:7], v[36:39], off
	global_store_dwordx4 v[6:7], v[40:43], off offset:16
	v_lshl_add_u64 v[6:7], v[6:7], 0, s[30:31]
	global_load_dwordx4 v[36:39], v[32:33], off
	global_load_dwordx4 v[40:43], v[32:33], off offset:16
	global_load_dword v44, v[26:27], off
	v_lshl_add_u64 v[32:33], v[32:33], 0, s[30:31]
	v_lshl_add_u64 v[26:27], v[26:27], 0, s[28:29]
	s_waitcnt vmcnt(3)
	s_nop 1
	v_add_f32_dpp v19, v45, v45 quad_perm:[1,0,3,2] row_mask:0xf bank_mask:0xf
	s_nop 1
	v_add_f32_dpp v18, v19, v19 quad_perm:[2,3,0,1] row_mask:0xf bank_mask:0xf
	s_nop 1
	v_add_f32_dpp v18, v18, v18 row_half_mirror row_mask:0xf bank_mask:0xf
	v_fmamk_f32 v18, v18, 0x39800000, v173
	v_mul_f32_e32 v19, 0x4f800000, v18
	v_cmp_gt_f32_e32 vcc, s51, v18
	s_nop 1
	v_cndmask_b32_e32 v18, v18, v19, vcc
	v_sqrt_f32_e32 v19, v18
	s_nop 0
	v_add_u32_e32 v20, -1, v19
	v_fma_f32 v22, -v20, v19, v18
	v_add_u32_e32 v21, 1, v19
	v_cmp_ge_f32_e64 s[14:15], 0, v22
	s_nop 1
	v_cndmask_b32_e64 v20, v19, v20, s[14:15]
	v_fma_f32 v19, -v21, v19, v18
	v_cmp_lt_f32_e64 s[14:15], 0, v19
	s_nop 1
	v_cndmask_b32_e64 v19, v20, v21, s[14:15]
	v_mul_f32_e32 v20, 0x37800000, v19
	v_cndmask_b32_e32 v19, v19, v20, vcc
	v_cmp_class_f32_e32 vcc, v18, v174
	s_nop 1
	v_cndmask_b32_e32 v18, v19, v18, vcc
	v_div_scale_f32 v19, s[14:15], v18, v18, 1.0
	v_rcp_f32_e32 v20, v19
	s_nop 0
	v_fma_f32 v21, -v19, v20, 1.0
	v_fmac_f32_e32 v20, v21, v20
	v_div_scale_f32 v21, vcc, 1.0, v18, 1.0
	v_mul_f32_e32 v22, v21, v20
	v_fma_f32 v23, -v19, v22, v21
	v_fmac_f32_e32 v22, v23, v20
	v_fma_f32 v19, -v19, v22, v21
	v_div_fmas_f32 v19, v19, v20, v22
	v_div_fixup_f32 v18, v19, v18, 1.0
	v_pk_mul_f32 v[10:11], v[10:11], v[18:19] op_sel_hi:[1,0]
	v_pk_mul_f32 v[12:13], v[12:13], v[18:19] op_sel_hi:[1,0]
	v_pk_mul_f32 v[14:15], v[14:15], v[18:19] op_sel_hi:[1,0]
	v_pk_mul_f32 v[16:17], v[16:17], v[18:19] op_sel_hi:[1,0]
	v_pk_mul_f32 v[10:11], v[10:11], v[100:101]
	v_pk_mul_f32 v[12:13], v[12:13], v[102:103]
	v_pk_mul_f32 v[14:15], v[14:15], v[104:105]
	v_pk_mul_f32 v[16:17], v[16:17], v[106:107]
	global_store_dwordx4 v[6:7], v[10:13], off
	global_store_dwordx4 v[6:7], v[14:17], off offset:16
	v_lshl_add_u64 v[6:7], v[6:7], 0, s[30:31]
	global_load_dwordx4 v[10:13], v[32:33], off
	global_load_dwordx4 v[14:17], v[32:33], off offset:16
	global_load_dword v45, v[26:27], off
	v_lshl_add_u64 v[32:33], v[32:33], 0, s[30:31]
	v_lshl_add_u64 v[26:27], v[26:27], 0, s[28:29]
	s_waitcnt vmcnt(3)
	s_nop 1
	v_add_f32_dpp v19, v44, v44 quad_perm:[1,0,3,2] row_mask:0xf bank_mask:0xf
	s_nop 1
	v_add_f32_dpp v18, v19, v19 quad_perm:[2,3,0,1] row_mask:0xf bank_mask:0xf
	s_nop 1
	v_add_f32_dpp v18, v18, v18 row_half_mirror row_mask:0xf bank_mask:0xf
	v_fmamk_f32 v18, v18, 0x39800000, v173
	v_mul_f32_e32 v19, 0x4f800000, v18
	v_cmp_gt_f32_e32 vcc, s51, v18
	s_nop 1
	v_cndmask_b32_e32 v18, v18, v19, vcc
	v_sqrt_f32_e32 v19, v18
	s_nop 0
	v_add_u32_e32 v20, -1, v19
	v_fma_f32 v22, -v20, v19, v18
	v_add_u32_e32 v21, 1, v19
	v_cmp_ge_f32_e64 s[14:15], 0, v22
	s_nop 1
	v_cndmask_b32_e64 v20, v19, v20, s[14:15]
	v_fma_f32 v19, -v21, v19, v18
	v_cmp_lt_f32_e64 s[14:15], 0, v19
	s_nop 1
	v_cndmask_b32_e64 v19, v20, v21, s[14:15]
	v_mul_f32_e32 v20, 0x37800000, v19
	v_cndmask_b32_e32 v19, v19, v20, vcc
	v_cmp_class_f32_e32 vcc, v18, v174
	s_nop 1
	v_cndmask_b32_e32 v18, v19, v18, vcc
	v_div_scale_f32 v19, s[14:15], v18, v18, 1.0
	v_rcp_f32_e32 v20, v19
	s_nop 0
	v_fma_f32 v21, -v19, v20, 1.0
	v_fmac_f32_e32 v20, v21, v20
	v_div_scale_f32 v21, vcc, 1.0, v18, 1.0
	v_mul_f32_e32 v22, v21, v20
	v_fma_f32 v23, -v19, v22, v21
	v_fmac_f32_e32 v22, v23, v20
	v_fma_f32 v19, -v19, v22, v21
	v_div_fmas_f32 v19, v19, v20, v22
	v_div_fixup_f32 v18, v19, v18, 1.0
	v_pk_mul_f32 v[36:37], v[36:37], v[18:19] op_sel_hi:[1,0]
	v_pk_mul_f32 v[38:39], v[38:39], v[18:19] op_sel_hi:[1,0]
	v_pk_mul_f32 v[40:41], v[40:41], v[18:19] op_sel_hi:[1,0]
	v_pk_mul_f32 v[42:43], v[42:43], v[18:19] op_sel_hi:[1,0]
	v_pk_mul_f32 v[36:37], v[36:37], v[100:101]
	v_pk_mul_f32 v[38:39], v[38:39], v[102:103]
	v_pk_mul_f32 v[40:41], v[40:41], v[104:105]
	v_pk_mul_f32 v[42:43], v[42:43], v[106:107]
	global_store_dwordx4 v[6:7], v[36:39], off
	global_store_dwordx4 v[6:7], v[40:43], off offset:16
	v_lshl_add_u64 v[6:7], v[6:7], 0, s[30:31]
	global_load_dwordx4 v[36:39], v[32:33], off
	global_load_dwordx4 v[40:43], v[32:33], off offset:16
	global_load_dword v44, v[26:27], off
	v_lshl_add_u64 v[32:33], v[32:33], 0, s[30:31]
	v_lshl_add_u64 v[26:27], v[26:27], 0, s[28:29]
	s_waitcnt vmcnt(3)
	s_nop 1
	v_add_f32_dpp v19, v45, v45 quad_perm:[1,0,3,2] row_mask:0xf bank_mask:0xf
	s_nop 1
	v_add_f32_dpp v18, v19, v19 quad_perm:[2,3,0,1] row_mask:0xf bank_mask:0xf
	s_nop 1
	v_add_f32_dpp v18, v18, v18 row_half_mirror row_mask:0xf bank_mask:0xf
	v_fmamk_f32 v18, v18, 0x39800000, v173
	v_mul_f32_e32 v19, 0x4f800000, v18
	v_cmp_gt_f32_e32 vcc, s51, v18
	s_nop 1
	v_cndmask_b32_e32 v18, v18, v19, vcc
	v_sqrt_f32_e32 v19, v18
	s_nop 0
	v_add_u32_e32 v20, -1, v19
	v_fma_f32 v22, -v20, v19, v18
	v_add_u32_e32 v21, 1, v19
	v_cmp_ge_f32_e64 s[14:15], 0, v22
	s_nop 1
	v_cndmask_b32_e64 v20, v19, v20, s[14:15]
	v_fma_f32 v19, -v21, v19, v18
	v_cmp_lt_f32_e64 s[14:15], 0, v19
	s_nop 1
	v_cndmask_b32_e64 v19, v20, v21, s[14:15]
	v_mul_f32_e32 v20, 0x37800000, v19
	v_cndmask_b32_e32 v19, v19, v20, vcc
	v_cmp_class_f32_e32 vcc, v18, v174
	s_nop 1
	v_cndmask_b32_e32 v18, v19, v18, vcc
	v_div_scale_f32 v19, s[14:15], v18, v18, 1.0
	v_rcp_f32_e32 v20, v19
	s_nop 0
	v_fma_f32 v21, -v19, v20, 1.0
	v_fmac_f32_e32 v20, v21, v20
	v_div_scale_f32 v21, vcc, 1.0, v18, 1.0
	v_mul_f32_e32 v22, v21, v20
	v_fma_f32 v23, -v19, v22, v21
	v_fmac_f32_e32 v22, v23, v20
	v_fma_f32 v19, -v19, v22, v21
	v_div_fmas_f32 v19, v19, v20, v22
	v_div_fixup_f32 v18, v19, v18, 1.0
	v_pk_mul_f32 v[10:11], v[10:11], v[18:19] op_sel_hi:[1,0]
	v_pk_mul_f32 v[12:13], v[12:13], v[18:19] op_sel_hi:[1,0]
	v_pk_mul_f32 v[14:15], v[14:15], v[18:19] op_sel_hi:[1,0]
	v_pk_mul_f32 v[16:17], v[16:17], v[18:19] op_sel_hi:[1,0]
	v_pk_mul_f32 v[10:11], v[10:11], v[100:101]
	v_pk_mul_f32 v[12:13], v[12:13], v[102:103]
	v_pk_mul_f32 v[14:15], v[14:15], v[104:105]
	v_pk_mul_f32 v[16:17], v[16:17], v[106:107]
	global_store_dwordx4 v[6:7], v[10:13], off
	global_store_dwordx4 v[6:7], v[14:17], off offset:16
	v_lshl_add_u64 v[6:7], v[6:7], 0, s[30:31]
	global_load_dwordx4 v[10:13], v[32:33], off
	global_load_dwordx4 v[14:17], v[32:33], off offset:16
	global_load_dword v45, v[26:27], off
	v_lshl_add_u64 v[32:33], v[32:33], 0, s[30:31]
	v_lshl_add_u64 v[26:27], v[26:27], 0, s[28:29]
	s_waitcnt vmcnt(3)
	s_nop 1
	v_add_f32_dpp v19, v44, v44 quad_perm:[1,0,3,2] row_mask:0xf bank_mask:0xf
	s_nop 1
	v_add_f32_dpp v18, v19, v19 quad_perm:[2,3,0,1] row_mask:0xf bank_mask:0xf
	s_nop 1
	v_add_f32_dpp v18, v18, v18 row_half_mirror row_mask:0xf bank_mask:0xf
	v_fmamk_f32 v18, v18, 0x39800000, v173
	v_mul_f32_e32 v19, 0x4f800000, v18
	v_cmp_gt_f32_e32 vcc, s51, v18
	s_nop 1
	v_cndmask_b32_e32 v18, v18, v19, vcc
	v_sqrt_f32_e32 v19, v18
	s_nop 0
	v_add_u32_e32 v20, -1, v19
	v_fma_f32 v22, -v20, v19, v18
	v_add_u32_e32 v21, 1, v19
	v_cmp_ge_f32_e64 s[14:15], 0, v22
	s_nop 1
	v_cndmask_b32_e64 v20, v19, v20, s[14:15]
	v_fma_f32 v19, -v21, v19, v18
	v_cmp_lt_f32_e64 s[14:15], 0, v19
	s_nop 1
	v_cndmask_b32_e64 v19, v20, v21, s[14:15]
	v_mul_f32_e32 v20, 0x37800000, v19
	v_cndmask_b32_e32 v19, v19, v20, vcc
	v_cmp_class_f32_e32 vcc, v18, v174
	s_nop 1
	v_cndmask_b32_e32 v18, v19, v18, vcc
	v_div_scale_f32 v19, s[14:15], v18, v18, 1.0
	v_rcp_f32_e32 v20, v19
	s_nop 0
	v_fma_f32 v21, -v19, v20, 1.0
	v_fmac_f32_e32 v20, v21, v20
	v_div_scale_f32 v21, vcc, 1.0, v18, 1.0
	v_mul_f32_e32 v22, v21, v20
	v_fma_f32 v23, -v19, v22, v21
	v_fmac_f32_e32 v22, v23, v20
	v_fma_f32 v19, -v19, v22, v21
	v_div_fmas_f32 v19, v19, v20, v22
	v_div_fixup_f32 v18, v19, v18, 1.0
	v_pk_mul_f32 v[36:37], v[36:37], v[18:19] op_sel_hi:[1,0]
	v_pk_mul_f32 v[38:39], v[38:39], v[18:19] op_sel_hi:[1,0]
	v_pk_mul_f32 v[40:41], v[40:41], v[18:19] op_sel_hi:[1,0]
	v_pk_mul_f32 v[42:43], v[42:43], v[18:19] op_sel_hi:[1,0]
	v_pk_mul_f32 v[36:37], v[36:37], v[100:101]
	v_pk_mul_f32 v[38:39], v[38:39], v[102:103]
	v_pk_mul_f32 v[40:41], v[40:41], v[104:105]
	v_pk_mul_f32 v[42:43], v[42:43], v[106:107]
	global_store_dwordx4 v[6:7], v[36:39], off
	global_store_dwordx4 v[6:7], v[40:43], off offset:16
	v_lshl_add_u64 v[6:7], v[6:7], 0, s[30:31]
	global_load_dwordx4 v[36:39], v[32:33], off
	global_load_dwordx4 v[40:43], v[32:33], off offset:16
	global_load_dword v44, v[26:27], off
	v_lshl_add_u64 v[32:33], v[32:33], 0, s[30:31]
	v_lshl_add_u64 v[26:27], v[26:27], 0, s[28:29]
	s_waitcnt vmcnt(3)
	s_nop 1
	v_add_f32_dpp v19, v45, v45 quad_perm:[1,0,3,2] row_mask:0xf bank_mask:0xf
	s_nop 1
	v_add_f32_dpp v18, v19, v19 quad_perm:[2,3,0,1] row_mask:0xf bank_mask:0xf
	s_nop 1
	v_add_f32_dpp v18, v18, v18 row_half_mirror row_mask:0xf bank_mask:0xf
	v_fmamk_f32 v18, v18, 0x39800000, v173
	v_mul_f32_e32 v19, 0x4f800000, v18
	v_cmp_gt_f32_e32 vcc, s51, v18
	s_nop 1
	v_cndmask_b32_e32 v18, v18, v19, vcc
	v_sqrt_f32_e32 v19, v18
	s_nop 0
	v_add_u32_e32 v20, -1, v19
	v_fma_f32 v22, -v20, v19, v18
	v_add_u32_e32 v21, 1, v19
	v_cmp_ge_f32_e64 s[14:15], 0, v22
	s_nop 1
	v_cndmask_b32_e64 v20, v19, v20, s[14:15]
	v_fma_f32 v19, -v21, v19, v18
	v_cmp_lt_f32_e64 s[14:15], 0, v19
	s_nop 1
	v_cndmask_b32_e64 v19, v20, v21, s[14:15]
	v_mul_f32_e32 v20, 0x37800000, v19
	v_cndmask_b32_e32 v19, v19, v20, vcc
	v_cmp_class_f32_e32 vcc, v18, v174
	s_nop 1
	v_cndmask_b32_e32 v18, v19, v18, vcc
	v_div_scale_f32 v19, s[14:15], v18, v18, 1.0
	v_rcp_f32_e32 v20, v19
	s_nop 0
	v_fma_f32 v21, -v19, v20, 1.0
	v_fmac_f32_e32 v20, v21, v20
	v_div_scale_f32 v21, vcc, 1.0, v18, 1.0
	v_mul_f32_e32 v22, v21, v20
	v_fma_f32 v23, -v19, v22, v21
	v_fmac_f32_e32 v22, v23, v20
	v_fma_f32 v19, -v19, v22, v21
	v_div_fmas_f32 v19, v19, v20, v22
	v_div_fixup_f32 v18, v19, v18, 1.0
	v_pk_mul_f32 v[10:11], v[10:11], v[18:19] op_sel_hi:[1,0]
	v_pk_mul_f32 v[12:13], v[12:13], v[18:19] op_sel_hi:[1,0]
	v_pk_mul_f32 v[14:15], v[14:15], v[18:19] op_sel_hi:[1,0]
	v_pk_mul_f32 v[16:17], v[16:17], v[18:19] op_sel_hi:[1,0]
	v_pk_mul_f32 v[10:11], v[10:11], v[100:101]
	v_pk_mul_f32 v[12:13], v[12:13], v[102:103]
	v_pk_mul_f32 v[14:15], v[14:15], v[104:105]
	v_pk_mul_f32 v[16:17], v[16:17], v[106:107]
	global_store_dwordx4 v[6:7], v[10:13], off
	global_store_dwordx4 v[6:7], v[14:17], off offset:16
	v_lshl_add_u64 v[6:7], v[6:7], 0, s[30:31]
	global_load_dwordx4 v[10:13], v[32:33], off
	global_load_dwordx4 v[14:17], v[32:33], off offset:16
	global_load_dword v45, v[26:27], off
	v_lshl_add_u64 v[32:33], v[32:33], 0, s[30:31]
	v_lshl_add_u64 v[26:27], v[26:27], 0, s[28:29]
	s_waitcnt vmcnt(3)
	s_nop 1
	v_add_f32_dpp v19, v44, v44 quad_perm:[1,0,3,2] row_mask:0xf bank_mask:0xf
	s_nop 1
	v_add_f32_dpp v18, v19, v19 quad_perm:[2,3,0,1] row_mask:0xf bank_mask:0xf
	s_nop 1
	v_add_f32_dpp v18, v18, v18 row_half_mirror row_mask:0xf bank_mask:0xf
	v_fmamk_f32 v18, v18, 0x39800000, v173
	v_mul_f32_e32 v19, 0x4f800000, v18
	v_cmp_gt_f32_e32 vcc, s51, v18
	s_nop 1
	v_cndmask_b32_e32 v18, v18, v19, vcc
	v_sqrt_f32_e32 v19, v18
	s_nop 0
	v_add_u32_e32 v20, -1, v19
	v_fma_f32 v22, -v20, v19, v18
	v_add_u32_e32 v21, 1, v19
	v_cmp_ge_f32_e64 s[14:15], 0, v22
	s_nop 1
	v_cndmask_b32_e64 v20, v19, v20, s[14:15]
	v_fma_f32 v19, -v21, v19, v18
	v_cmp_lt_f32_e64 s[14:15], 0, v19
	s_nop 1
	v_cndmask_b32_e64 v19, v20, v21, s[14:15]
	v_mul_f32_e32 v20, 0x37800000, v19
	v_cndmask_b32_e32 v19, v19, v20, vcc
	v_cmp_class_f32_e32 vcc, v18, v174
	s_nop 1
	v_cndmask_b32_e32 v18, v19, v18, vcc
	v_div_scale_f32 v19, s[14:15], v18, v18, 1.0
	v_rcp_f32_e32 v20, v19
	s_nop 0
	v_fma_f32 v21, -v19, v20, 1.0
	v_fmac_f32_e32 v20, v21, v20
	v_div_scale_f32 v21, vcc, 1.0, v18, 1.0
	v_mul_f32_e32 v22, v21, v20
	v_fma_f32 v23, -v19, v22, v21
	v_fmac_f32_e32 v22, v23, v20
	v_fma_f32 v19, -v19, v22, v21
	v_div_fmas_f32 v19, v19, v20, v22
	v_div_fixup_f32 v18, v19, v18, 1.0
	v_pk_mul_f32 v[36:37], v[36:37], v[18:19] op_sel_hi:[1,0]
	v_pk_mul_f32 v[38:39], v[38:39], v[18:19] op_sel_hi:[1,0]
	v_pk_mul_f32 v[40:41], v[40:41], v[18:19] op_sel_hi:[1,0]
	v_pk_mul_f32 v[42:43], v[42:43], v[18:19] op_sel_hi:[1,0]
	v_pk_mul_f32 v[36:37], v[36:37], v[100:101]
	v_pk_mul_f32 v[38:39], v[38:39], v[102:103]
	v_pk_mul_f32 v[40:41], v[40:41], v[104:105]
	v_pk_mul_f32 v[42:43], v[42:43], v[106:107]
	global_store_dwordx4 v[6:7], v[36:39], off
	global_store_dwordx4 v[6:7], v[40:43], off offset:16
	v_lshl_add_u64 v[6:7], v[6:7], 0, s[30:31]
	global_load_dwordx4 v[36:39], v[32:33], off
	global_load_dwordx4 v[40:43], v[32:33], off offset:16
	global_load_dword v44, v[26:27], off
	v_lshl_add_u64 v[32:33], v[32:33], 0, s[30:31]
	v_lshl_add_u64 v[26:27], v[26:27], 0, s[28:29]
	s_waitcnt vmcnt(3)
	s_nop 1
	v_add_f32_dpp v19, v45, v45 quad_perm:[1,0,3,2] row_mask:0xf bank_mask:0xf
	s_nop 1
	v_add_f32_dpp v18, v19, v19 quad_perm:[2,3,0,1] row_mask:0xf bank_mask:0xf
	s_nop 1
	v_add_f32_dpp v18, v18, v18 row_half_mirror row_mask:0xf bank_mask:0xf
	v_fmamk_f32 v18, v18, 0x39800000, v173
	v_mul_f32_e32 v19, 0x4f800000, v18
	v_cmp_gt_f32_e32 vcc, s51, v18
	s_nop 1
	v_cndmask_b32_e32 v18, v18, v19, vcc
	v_sqrt_f32_e32 v19, v18
	s_nop 0
	v_add_u32_e32 v20, -1, v19
	v_fma_f32 v22, -v20, v19, v18
	v_add_u32_e32 v21, 1, v19
	v_cmp_ge_f32_e64 s[14:15], 0, v22
	s_nop 1
	v_cndmask_b32_e64 v20, v19, v20, s[14:15]
	v_fma_f32 v19, -v21, v19, v18
	v_cmp_lt_f32_e64 s[14:15], 0, v19
	s_nop 1
	v_cndmask_b32_e64 v19, v20, v21, s[14:15]
	v_mul_f32_e32 v20, 0x37800000, v19
	v_cndmask_b32_e32 v19, v19, v20, vcc
	v_cmp_class_f32_e32 vcc, v18, v174
	s_nop 1
	v_cndmask_b32_e32 v18, v19, v18, vcc
	v_div_scale_f32 v19, s[14:15], v18, v18, 1.0
	v_rcp_f32_e32 v20, v19
	s_nop 0
	v_fma_f32 v21, -v19, v20, 1.0
	v_fmac_f32_e32 v20, v21, v20
	v_div_scale_f32 v21, vcc, 1.0, v18, 1.0
	v_mul_f32_e32 v22, v21, v20
	v_fma_f32 v23, -v19, v22, v21
	v_fmac_f32_e32 v22, v23, v20
	v_fma_f32 v19, -v19, v22, v21
	v_div_fmas_f32 v19, v19, v20, v22
	v_div_fixup_f32 v18, v19, v18, 1.0
	v_pk_mul_f32 v[10:11], v[10:11], v[18:19] op_sel_hi:[1,0]
	v_pk_mul_f32 v[12:13], v[12:13], v[18:19] op_sel_hi:[1,0]
	v_pk_mul_f32 v[14:15], v[14:15], v[18:19] op_sel_hi:[1,0]
	v_pk_mul_f32 v[16:17], v[16:17], v[18:19] op_sel_hi:[1,0]
	v_pk_mul_f32 v[10:11], v[10:11], v[100:101]
	v_pk_mul_f32 v[12:13], v[12:13], v[102:103]
	v_pk_mul_f32 v[14:15], v[14:15], v[104:105]
	v_pk_mul_f32 v[16:17], v[16:17], v[106:107]
	global_store_dwordx4 v[6:7], v[10:13], off
	global_store_dwordx4 v[6:7], v[14:17], off offset:16
	v_lshl_add_u64 v[6:7], v[6:7], 0, s[30:31]
	s_waitcnt vmcnt(0)
	s_nop 1
	v_add_f32_dpp v19, v44, v44 quad_perm:[1,0,3,2] row_mask:0xf bank_mask:0xf
	s_nop 1
	v_add_f32_dpp v18, v19, v19 quad_perm:[2,3,0,1] row_mask:0xf bank_mask:0xf
	s_nop 1
	v_add_f32_dpp v18, v18, v18 row_half_mirror row_mask:0xf bank_mask:0xf
	v_fmamk_f32 v18, v18, 0x39800000, v173
	v_mul_f32_e32 v19, 0x4f800000, v18
	v_cmp_gt_f32_e32 vcc, s51, v18
	s_nop 1
	v_cndmask_b32_e32 v18, v18, v19, vcc
	v_sqrt_f32_e32 v19, v18
	s_nop 0
	v_add_u32_e32 v20, -1, v19
	v_fma_f32 v22, -v20, v19, v18
	v_add_u32_e32 v21, 1, v19
	v_cmp_ge_f32_e64 s[14:15], 0, v22
	s_nop 1
	v_cndmask_b32_e64 v20, v19, v20, s[14:15]
	v_fma_f32 v19, -v21, v19, v18
	v_cmp_lt_f32_e64 s[14:15], 0, v19
	s_nop 1
	v_cndmask_b32_e64 v19, v20, v21, s[14:15]
	v_mul_f32_e32 v20, 0x37800000, v19
	v_cndmask_b32_e32 v19, v19, v20, vcc
	v_cmp_class_f32_e32 vcc, v18, v174
	s_nop 1
	v_cndmask_b32_e32 v18, v19, v18, vcc
	v_div_scale_f32 v19, s[14:15], v18, v18, 1.0
	v_rcp_f32_e32 v20, v19
	s_nop 0
	v_fma_f32 v21, -v19, v20, 1.0
	v_fmac_f32_e32 v20, v21, v20
	v_div_scale_f32 v21, vcc, 1.0, v18, 1.0
	v_mul_f32_e32 v22, v21, v20
	v_fma_f32 v23, -v19, v22, v21
	v_fmac_f32_e32 v22, v23, v20
	v_fma_f32 v19, -v19, v22, v21
	v_div_fmas_f32 v19, v19, v20, v22
	v_div_fixup_f32 v18, v19, v18, 1.0
	v_pk_mul_f32 v[36:37], v[36:37], v[18:19] op_sel_hi:[1,0]
	v_pk_mul_f32 v[38:39], v[38:39], v[18:19] op_sel_hi:[1,0]
	v_pk_mul_f32 v[40:41], v[40:41], v[18:19] op_sel_hi:[1,0]
	v_pk_mul_f32 v[42:43], v[42:43], v[18:19] op_sel_hi:[1,0]
	v_pk_mul_f32 v[36:37], v[36:37], v[100:101]
	v_pk_mul_f32 v[38:39], v[38:39], v[102:103]
	v_pk_mul_f32 v[40:41], v[40:41], v[104:105]
	v_pk_mul_f32 v[42:43], v[42:43], v[106:107]
	global_store_dwordx4 v[6:7], v[36:39], off
	global_store_dwordx4 v[6:7], v[40:43], off offset:16
	v_lshl_add_u64 v[6:7], v[6:7], 0, s[30:31]
	s_waitcnt vmcnt(0)
	s_branch .LBB0_1485
	s_cmp_gt_i32 s56, 12
	s_cselect_b64 s[2:3], -1, 0
	s_cmp_lt_i32 s57, 13
	s_cselect_b64 s[4:5], -1, 0
	s_or_b64 s[2:3], s[2:3], s[4:5]
	s_and_b64 vcc, exec, s[2:3]
	s_cbranch_vccnz .LBB0_1485
	s_load_dword s25, s[0:1], 0xd8
	s_waitcnt lgkmcnt(0)
	s_and_b32 s2, s25, 7
	s_cmp_lg_u32 s2, 0
	v_readfirstlane_b32 s2, v0
	s_cbranch_scc1 .LBB0_1466
	s_ashr_i32 s4, s33, 31
	s_lshr_b32 s4, s4, 29
	s_add_i32 s4, s33, s4
	s_ashr_i32 s5, s4, 3
	s_and_b32 s4, s4, -8
	s_ashr_i32 s3, s25, 3
	s_sub_i32 s4, s33, s4
	s_mul_i32 s3, s3, s4
	s_add_i32 s33, s3, s5
